# gather-prep slot loop: block residue carried incrementally instead of a magic division per value, unit match skips units 4..7 when the workgroup has at most four; stacked
# speedup vs baseline: 1.0014x; 1.0014x over previous
.LBB0_762:
	s_or_b64 exec, exec, s[0:1]
	s_abs_i32 s11, s80
	v_cvt_f32_u32_e32 v1, s11
	v_mov_b32_e32 v11, 0
	s_sub_i32 s0, 0, s11
	s_waitcnt lgkmcnt(0)
	v_rcp_iflag_f32_e32 v1, v1
	s_barrier
	ds_read_b128 v[2:5], v11 offset:37120
	ds_read_b128 v[6:9], v11 offset:37136
	v_mul_f32_e32 v1, 0x4f7ffffe, v1
	v_cvt_u32_f32_e32 v1, v1
	v_lshrrev_b32_e32 v14, 6, v0
	v_lshrrev_b32_e32 v15, 7, v0
	s_movk_i32 s12, 0xfe00
	v_mul_lo_u32 v10, s0, v1
	v_mul_hi_u32 v10, v1, v10
	v_add_u32_e32 v16, v1, v10
	v_lshlrev_b32_e32 v10, 2, v0
	v_lshl_add_u64 v[12:13], s[28:29], 0, v[10:11]
	s_mov_b64 s[0:1], 0x110000
	v_and_b32_e32 v1, 0x180, v0
	v_lshl_add_u64 v[12:13], v[12:13], 0, s[0:1]
	v_add_u32_e32 v11, 0, v1
	s_mov_b64 s[0:1], 0
	s_add_i32 s10, 0, 0x22000
	s_mov_b64 s[6:7], 0x800
	s_movk_i32 s13, 0x7dff
	v_mov_b32_e32 v17, 2
	v_mov_b32_e32 v18, v34
	s_add_u32 s12, s28, 0x110000
	s_addc_u32 s13, s29, 0
	s_add_u32 s16, s28, 0x150000
	s_addc_u32 s17, s29, 0
	v_lshrrev_b32_e32 v36, 7, v0
	v_mov_b32_e32 v104, 0x0
	v_mov_b32_e32 v105, 0x400
	v_mov_b32_e32 v106, 0x800
	v_mov_b32_e32 v107, 0xc00
	v_mov_b32_e32 v108, 0x1000
	v_mov_b32_e32 v109, 0x1400
	v_mov_b32_e32 v110, 0x1800
	v_mov_b32_e32 v111, 0x1c00
	global_load_dword v40, v10, s[12:13]
	v_add_u32_e32 v1, 0x800, v10
	global_load_dword v41, v1, s[12:13]
	v_add_u32_e32 v1, 0x1000, v10
	global_load_dword v42, v1, s[12:13]
	v_add_u32_e32 v1, 0x1800, v10
	global_load_dword v43, v1, s[12:13]
	v_add_u32_e32 v1, 0x2000, v10
	global_load_dword v44, v1, s[12:13]
	v_add_u32_e32 v1, 0x2800, v10
	global_load_dword v45, v1, s[12:13]
	v_add_u32_e32 v1, 0x3000, v10
	global_load_dword v46, v1, s[12:13]
	v_add_u32_e32 v1, 0x3800, v10
	global_load_dword v47, v1, s[12:13]
	v_add_u32_e32 v1, 0x4000, v10
	global_load_dword v48, v1, s[12:13]
	v_add_u32_e32 v1, 0x4800, v10
	global_load_dword v49, v1, s[12:13]
	v_add_u32_e32 v1, 0x5000, v10
	global_load_dword v50, v1, s[12:13]
	v_add_u32_e32 v1, 0x5800, v10
	global_load_dword v51, v1, s[12:13]
	v_add_u32_e32 v1, 0x6000, v10
	global_load_dword v52, v1, s[12:13]
	v_add_u32_e32 v1, 0x6800, v10
	global_load_dword v53, v1, s[12:13]
	v_add_u32_e32 v1, 0x7000, v10
	global_load_dword v54, v1, s[12:13]
	v_add_u32_e32 v1, 0x7800, v10
	global_load_dword v55, v1, s[12:13]
	v_add_u32_e32 v1, 0x8000, v10
	global_load_dword v56, v1, s[12:13]
	v_add_u32_e32 v1, 0x8800, v10
	global_load_dword v57, v1, s[12:13]
	v_add_u32_e32 v1, 0x9000, v10
	global_load_dword v58, v1, s[12:13]
	v_add_u32_e32 v1, 0x9800, v10
	global_load_dword v59, v1, s[12:13]
	v_add_u32_e32 v1, 0xa000, v10
	global_load_dword v60, v1, s[12:13]
	v_add_u32_e32 v1, 0xa800, v10
	global_load_dword v61, v1, s[12:13]
	v_add_u32_e32 v1, 0xb000, v10
	global_load_dword v62, v1, s[12:13]
	v_add_u32_e32 v1, 0xb800, v10
	global_load_dword v63, v1, s[12:13]
	v_add_u32_e32 v1, 0xc000, v10
	global_load_dword v64, v1, s[12:13]
	v_add_u32_e32 v1, 0xc800, v10
	global_load_dword v65, v1, s[12:13]
	v_add_u32_e32 v1, 0xd000, v10
	global_load_dword v66, v1, s[12:13]
	v_add_u32_e32 v1, 0xd800, v10
	global_load_dword v67, v1, s[12:13]
	v_add_u32_e32 v1, 0xe000, v10
	global_load_dword v68, v1, s[12:13]
	v_add_u32_e32 v1, 0xe800, v10
	global_load_dword v69, v1, s[12:13]
	v_add_u32_e32 v1, 0xf000, v10
	global_load_dword v70, v1, s[12:13]
	v_add_u32_e32 v1, 0xf800, v10
	global_load_dword v71, v1, s[12:13]
	v_add_u32_e32 v1, 0x10000, v10
	global_load_dword v72, v1, s[12:13]
	v_add_u32_e32 v1, 0x10800, v10
	global_load_dword v73, v1, s[12:13]
	v_add_u32_e32 v1, 0x11000, v10
	global_load_dword v74, v1, s[12:13]
	v_add_u32_e32 v1, 0x11800, v10
	global_load_dword v75, v1, s[12:13]
	v_add_u32_e32 v1, 0x12000, v10
	global_load_dword v76, v1, s[12:13]
	v_add_u32_e32 v1, 0x12800, v10
	global_load_dword v77, v1, s[12:13]
	v_add_u32_e32 v1, 0x13000, v10
	global_load_dword v78, v1, s[12:13]
	v_add_u32_e32 v1, 0x13800, v10
	global_load_dword v79, v1, s[12:13]
	v_add_u32_e32 v1, 0x14000, v10
	global_load_dword v80, v1, s[12:13]
	v_add_u32_e32 v1, 0x14800, v10
	global_load_dword v81, v1, s[12:13]
	v_add_u32_e32 v1, 0x15000, v10
	global_load_dword v82, v1, s[12:13]
	v_add_u32_e32 v1, 0x15800, v10
	global_load_dword v83, v1, s[12:13]
	v_add_u32_e32 v1, 0x16000, v10
	global_load_dword v84, v1, s[12:13]
	v_add_u32_e32 v1, 0x16800, v10
	global_load_dword v85, v1, s[12:13]
	v_add_u32_e32 v1, 0x17000, v10
	global_load_dword v86, v1, s[12:13]
	v_add_u32_e32 v1, 0x17800, v10
	global_load_dword v87, v1, s[12:13]
	s_waitcnt vmcnt(32)
	v_add_u32_e32 v1, 0x18000, v10
	global_load_dword v88, v1, s[12:13]
	v_add_u32_e32 v1, 0x18800, v10
	global_load_dword v89, v1, s[12:13]
	v_add_u32_e32 v1, 0x19000, v10
	global_load_dword v90, v1, s[12:13]
	v_add_u32_e32 v1, 0x19800, v10
	global_load_dword v91, v1, s[12:13]
	v_add_u32_e32 v1, 0x1a000, v10
	global_load_dword v92, v1, s[12:13]
	v_add_u32_e32 v1, 0x1a800, v10
	global_load_dword v93, v1, s[12:13]
	v_add_u32_e32 v1, 0x1b000, v10
	global_load_dword v94, v1, s[12:13]
	v_add_u32_e32 v1, 0x1b800, v10
	global_load_dword v95, v1, s[12:13]
	v_add_u32_e32 v1, 0x1c000, v10
	global_load_dword v96, v1, s[12:13]
	v_add_u32_e32 v1, 0x1c800, v10
	global_load_dword v97, v1, s[12:13]
	v_add_u32_e32 v1, 0x1d000, v10
	global_load_dword v98, v1, s[12:13]
	v_add_u32_e32 v1, 0x1d800, v10
	global_load_dword v99, v1, s[12:13]
	v_add_u32_e32 v1, 0x1e000, v10
	global_load_dword v100, v1, s[12:13]
	v_add_u32_e32 v1, 0x1e800, v10
	global_load_dword v101, v1, s[12:13]
	v_add_u32_e32 v1, 0x1f000, v10
	global_load_dword v102, v1, s[12:13]
	v_add_u32_e32 v1, 0x1f800, v10
	global_load_dword v103, v1, s[12:13]
	s_waitcnt lgkmcnt(0)
	v_mul_hi_u32 v37, v36, v16
	v_mul_lo_u32 v37, v37, s11
	v_sub_u32_e32 v37, v36, v37
	v_subrev_u32_e32 v1, s11, v37
	v_min_u32_e32 v37, v37, v1
	v_subrev_u32_e32 v1, s11, v37
	v_min_u32_e32 v37, v37, v1
	s_waitcnt vmcnt(0)
	v_and_b32_e32 v112, 0xff, v40
	v_and_b32_e32 v120, 0xff, v41
	v_and_b32_e32 v128, 0xff, v42
	v_and_b32_e32 v136, 0xff, v43
	v_lshlrev_b32_e32 v112, 2, v112
	v_lshlrev_b32_e32 v120, 2, v120
	v_lshlrev_b32_e32 v128, 2, v128
	v_lshlrev_b32_e32 v136, 2, v136
	v_add_u32_e32 v118, v112, v11
	v_add_u32_e32 v126, v120, v11
	v_add_u32_e32 v134, v128, v11
	v_add_u32_e32 v142, v136, v11
	ds_read_b32 v113, v112 offset:36864
	ds_read_b32 v114, v112 offset:34816
	ds_read_b32 v115, v118
	ds_read_b32 v121, v120 offset:36864
	ds_read_b32 v122, v120 offset:34816
	ds_read_b32 v123, v126 offset:512
	ds_read_b32 v129, v128 offset:36864
	ds_read_b32 v130, v128 offset:34816
	ds_read_b32 v131, v134 offset:1024
	ds_read_b32 v137, v136 offset:36864
	ds_read_b32 v138, v136 offset:34816
	ds_read_b32 v139, v142 offset:1536
	v_mov_b32_e32 v117, v37
	v_add_u32_e32 v37, 4, v37
	v_subrev_u32_e32 v118, s11, v37
	v_min_u32_e32 v37, v37, v118
	v_subrev_u32_e32 v118, s11, v37
	v_min_u32_e32 v37, v37, v118
	v_mov_b32_e32 v125, v37
	v_add_u32_e32 v37, 4, v37
	v_subrev_u32_e32 v126, s11, v37
	v_min_u32_e32 v37, v37, v126
	v_subrev_u32_e32 v126, s11, v37
	v_min_u32_e32 v37, v37, v126
	v_mov_b32_e32 v133, v37
	v_add_u32_e32 v37, 4, v37
	v_subrev_u32_e32 v134, s11, v37
	v_min_u32_e32 v37, v37, v134
	v_subrev_u32_e32 v134, s11, v37
	v_min_u32_e32 v37, v37, v134
	v_mov_b32_e32 v141, v37
	v_add_u32_e32 v37, 4, v37
	v_subrev_u32_e32 v142, s11, v37
	v_min_u32_e32 v37, v37, v142
	v_subrev_u32_e32 v142, s11, v37
	v_min_u32_e32 v37, v37, v142
	v_ashrrev_i32_e32 v116, 8, v40
	v_ashrrev_i32_e32 v124, 8, v41
	v_ashrrev_i32_e32 v132, 8, v42
	v_ashrrev_i32_e32 v140, 8, v43
	s_waitcnt lgkmcnt(0)
	v_add_u32_e32 v116, v116, v113
	v_add_u32_e32 v124, v124, v121
	v_add_u32_e32 v132, v132, v129
	v_add_u32_e32 v140, v140, v137
	v_add3_u32 v116, v116, v114, v115
	v_add3_u32 v124, v124, v122, v123
	v_add3_u32 v132, v132, v130, v131
	v_add3_u32 v140, v140, v138, v139
	v_cmp_eq_u32_e32 vcc, s93, v117
	v_mov_b32_e32 v1, v10
	s_and_saveexec_b64 s[24:25], vcc
	global_store_dword v1, v116, s[16:17]
	s_mov_b64 exec, s[24:25]
	v_cmp_eq_u32_e32 vcc, s93, v125
	v_add_u32_e32 v1, 0x800, v10
	s_and_saveexec_b64 s[24:25], vcc
	global_store_dword v1, v124, s[16:17]
	s_mov_b64 exec, s[24:25]
	v_cmp_eq_u32_e32 vcc, s93, v133
	v_add_u32_e32 v1, 0x1000, v10
	s_and_saveexec_b64 s[24:25], vcc
	global_store_dword v1, v132, s[16:17]
	s_mov_b64 exec, s[24:25]
	v_cmp_eq_u32_e32 vcc, s93, v141
	v_add_u32_e32 v1, 0x1800, v10
	s_and_saveexec_b64 s[24:25], vcc
	global_store_dword v1, v140, s[16:17]
	s_mov_b64 exec, s[24:25]
	v_ashrrev_i32_e32 v113, 8, v116
	v_ashrrev_i32_e32 v121, 8, v124
	v_ashrrev_i32_e32 v129, 8, v132
	v_ashrrev_i32_e32 v137, 8, v140
	v_and_b32_e32 v112, 0xff, v116
	v_and_b32_e32 v120, 0xff, v124
	v_and_b32_e32 v128, 0xff, v132
	v_and_b32_e32 v136, 0xff, v140
	v_lshl_add_u32 v112, v112, 2, s10
	v_lshl_add_u32 v120, v120, 2, s10
	v_lshl_add_u32 v128, v128, 2, s10
	v_lshl_add_u32 v136, v136, 2, s10
	v_mov_b32_e32 v114, v34
	v_add_u32_e32 v122, 0x100, v34
	v_add_u32_e32 v130, 0x200, v34
	v_add_u32_e32 v138, 0x300, v34
	v_mov_b32_e32 v119, -1
	v_mov_b32_e32 v127, -1
	v_mov_b32_e32 v135, -1
	v_mov_b32_e32 v143, -1
	v_cmp_eq_u32_e32 vcc, v113, v2
	v_cmp_eq_u32_e64 s[0:1], v121, v2
	v_cmp_eq_u32_e64 s[6:7], v129, v2
	v_cmp_eq_u32_e64 s[8:9], v137, v2
	v_cndmask_b32_e32 v119, v119, v104, vcc
	v_cndmask_b32_e64 v127, v127, v104, s[0:1]
	v_cndmask_b32_e64 v135, v135, v104, s[6:7]
	v_cndmask_b32_e64 v143, v143, v104, s[8:9]
	v_cmp_eq_u32_e32 vcc, v113, v3
	v_cmp_eq_u32_e64 s[0:1], v121, v3
	v_cmp_eq_u32_e64 s[6:7], v129, v3
	v_cmp_eq_u32_e64 s[8:9], v137, v3
	v_cndmask_b32_e32 v119, v119, v105, vcc
	v_cndmask_b32_e64 v127, v127, v105, s[0:1]
	v_cndmask_b32_e64 v135, v135, v105, s[6:7]
	v_cndmask_b32_e64 v143, v143, v105, s[8:9]
	v_cmp_eq_u32_e32 vcc, v113, v4
	v_cmp_eq_u32_e64 s[0:1], v121, v4
	v_cmp_eq_u32_e64 s[6:7], v129, v4
	v_cmp_eq_u32_e64 s[8:9], v137, v4
	v_cndmask_b32_e32 v119, v119, v106, vcc
	v_cndmask_b32_e64 v127, v127, v106, s[0:1]
	v_cndmask_b32_e64 v135, v135, v106, s[6:7]
	v_cndmask_b32_e64 v143, v143, v106, s[8:9]
	v_cmp_eq_u32_e32 vcc, v113, v5
	v_cmp_eq_u32_e64 s[0:1], v121, v5
	v_cmp_eq_u32_e64 s[6:7], v129, v5
	v_cmp_eq_u32_e64 s[8:9], v137, v5
	v_cndmask_b32_e32 v119, v119, v107, vcc
	v_cndmask_b32_e64 v127, v127, v107, s[0:1]
	v_cndmask_b32_e64 v135, v135, v107, s[6:7]
	v_cndmask_b32_e64 v143, v143, v107, s[8:9]
	v_cmp_gt_i32_e32 vcc, 0, v6
	s_cbranch_vccnz .Lprep_a_m0
	v_cmp_eq_u32_e32 vcc, v113, v6
	v_cmp_eq_u32_e64 s[0:1], v121, v6
	v_cmp_eq_u32_e64 s[6:7], v129, v6
	v_cmp_eq_u32_e64 s[8:9], v137, v6
	v_cndmask_b32_e32 v119, v119, v108, vcc
	v_cndmask_b32_e64 v127, v127, v108, s[0:1]
	v_cndmask_b32_e64 v135, v135, v108, s[6:7]
	v_cndmask_b32_e64 v143, v143, v108, s[8:9]
	v_cmp_eq_u32_e32 vcc, v113, v7
	v_cmp_eq_u32_e64 s[0:1], v121, v7
	v_cmp_eq_u32_e64 s[6:7], v129, v7
	v_cmp_eq_u32_e64 s[8:9], v137, v7
	v_cndmask_b32_e32 v119, v119, v109, vcc
	v_cndmask_b32_e64 v127, v127, v109, s[0:1]
	v_cndmask_b32_e64 v135, v135, v109, s[6:7]
	v_cndmask_b32_e64 v143, v143, v109, s[8:9]
	v_cmp_eq_u32_e32 vcc, v113, v8
	v_cmp_eq_u32_e64 s[0:1], v121, v8
	v_cmp_eq_u32_e64 s[6:7], v129, v8
	v_cmp_eq_u32_e64 s[8:9], v137, v8
	v_cndmask_b32_e32 v119, v119, v110, vcc
	v_cndmask_b32_e64 v127, v127, v110, s[0:1]
	v_cndmask_b32_e64 v135, v135, v110, s[6:7]
	v_cndmask_b32_e64 v143, v143, v110, s[8:9]
	v_cmp_eq_u32_e32 vcc, v113, v9
	v_cmp_eq_u32_e64 s[0:1], v121, v9
	v_cmp_eq_u32_e64 s[6:7], v129, v9
	v_cmp_eq_u32_e64 s[8:9], v137, v9
	v_cndmask_b32_e32 v119, v119, v111, vcc
	v_cndmask_b32_e64 v127, v127, v111, s[0:1]
	v_cndmask_b32_e64 v135, v135, v111, s[6:7]
	v_cndmask_b32_e64 v143, v143, v111, s[8:9]
.Lprep_a_m0:
	v_add_u32_e32 v112, v112, v119
	v_add_u32_e32 v120, v120, v127
	v_add_u32_e32 v128, v128, v135
	v_add_u32_e32 v136, v136, v143
	v_cmp_ne_u32_e32 vcc, -1, v119
	s_and_saveexec_b64 s[24:25], vcc
	ds_write_b32 v112, v114
	s_mov_b64 exec, s[24:25]
	v_cmp_ne_u32_e32 vcc, -1, v127
	s_and_saveexec_b64 s[24:25], vcc
	ds_write_b32 v120, v122
	s_mov_b64 exec, s[24:25]
	v_cmp_ne_u32_e32 vcc, -1, v135
	s_and_saveexec_b64 s[24:25], vcc
	ds_write_b32 v128, v130
	s_mov_b64 exec, s[24:25]
	v_cmp_ne_u32_e32 vcc, -1, v143
	s_and_saveexec_b64 s[24:25], vcc
	ds_write_b32 v136, v138
	s_mov_b64 exec, s[24:25]
	v_and_b32_e32 v112, 0xff, v44
	v_and_b32_e32 v120, 0xff, v45
	v_and_b32_e32 v128, 0xff, v46
	v_and_b32_e32 v136, 0xff, v47
	v_lshlrev_b32_e32 v112, 2, v112
	v_lshlrev_b32_e32 v120, 2, v120
	v_lshlrev_b32_e32 v128, 2, v128
	v_lshlrev_b32_e32 v136, 2, v136
	v_add_u32_e32 v118, v112, v11
	v_add_u32_e32 v126, v120, v11
	v_add_u32_e32 v134, v128, v11
	v_add_u32_e32 v142, v136, v11
	ds_read_b32 v113, v112 offset:36864
	ds_read_b32 v114, v112 offset:34944
	ds_read_b32 v115, v118 offset:2048
	ds_read_b32 v121, v120 offset:36864
	ds_read_b32 v122, v120 offset:34944
	ds_read_b32 v123, v126 offset:2560
	ds_read_b32 v129, v128 offset:36864
	ds_read_b32 v130, v128 offset:34944
	ds_read_b32 v131, v134 offset:3072
	ds_read_b32 v137, v136 offset:36864
	ds_read_b32 v138, v136 offset:34944
	ds_read_b32 v139, v142 offset:3584
	v_mov_b32_e32 v117, v37
	v_add_u32_e32 v37, 4, v37
	v_subrev_u32_e32 v118, s11, v37
	v_min_u32_e32 v37, v37, v118
	v_subrev_u32_e32 v118, s11, v37
	v_min_u32_e32 v37, v37, v118
	v_mov_b32_e32 v125, v37
	v_add_u32_e32 v37, 4, v37
	v_subrev_u32_e32 v126, s11, v37
	v_min_u32_e32 v37, v37, v126
	v_subrev_u32_e32 v126, s11, v37
	v_min_u32_e32 v37, v37, v126
	v_mov_b32_e32 v133, v37
	v_add_u32_e32 v37, 4, v37
	v_subrev_u32_e32 v134, s11, v37
	v_min_u32_e32 v37, v37, v134
	v_subrev_u32_e32 v134, s11, v37
	v_min_u32_e32 v37, v37, v134
	v_mov_b32_e32 v141, v37
	v_add_u32_e32 v37, 4, v37
	v_subrev_u32_e32 v142, s11, v37
	v_min_u32_e32 v37, v37, v142
	v_subrev_u32_e32 v142, s11, v37
	v_min_u32_e32 v37, v37, v142
	v_ashrrev_i32_e32 v116, 8, v44
	v_ashrrev_i32_e32 v124, 8, v45
	v_ashrrev_i32_e32 v132, 8, v46
	v_ashrrev_i32_e32 v140, 8, v47
	s_waitcnt lgkmcnt(0)
	v_add_u32_e32 v116, v116, v113
	v_add_u32_e32 v124, v124, v121
	v_add_u32_e32 v132, v132, v129
	v_add_u32_e32 v140, v140, v137
	v_add3_u32 v116, v116, v114, v115
	v_add3_u32 v124, v124, v122, v123
	v_add3_u32 v132, v132, v130, v131
	v_add3_u32 v140, v140, v138, v139
	v_cmp_eq_u32_e32 vcc, s93, v117
	v_add_u32_e32 v1, 0x2000, v10
	s_and_saveexec_b64 s[24:25], vcc
	global_store_dword v1, v116, s[16:17]
	s_mov_b64 exec, s[24:25]
	v_cmp_eq_u32_e32 vcc, s93, v125
	v_add_u32_e32 v1, 0x2800, v10
	s_and_saveexec_b64 s[24:25], vcc
	global_store_dword v1, v124, s[16:17]
	s_mov_b64 exec, s[24:25]
	v_cmp_eq_u32_e32 vcc, s93, v133
	v_add_u32_e32 v1, 0x3000, v10
	s_and_saveexec_b64 s[24:25], vcc
	global_store_dword v1, v132, s[16:17]
	s_mov_b64 exec, s[24:25]
	v_cmp_eq_u32_e32 vcc, s93, v141
	v_add_u32_e32 v1, 0x3800, v10
	s_and_saveexec_b64 s[24:25], vcc
	global_store_dword v1, v140, s[16:17]
	s_mov_b64 exec, s[24:25]
	v_ashrrev_i32_e32 v113, 8, v116
	v_ashrrev_i32_e32 v121, 8, v124
	v_ashrrev_i32_e32 v129, 8, v132
	v_ashrrev_i32_e32 v137, 8, v140
	v_and_b32_e32 v112, 0xff, v116
	v_and_b32_e32 v120, 0xff, v124
	v_and_b32_e32 v128, 0xff, v132
	v_and_b32_e32 v136, 0xff, v140
	v_lshl_add_u32 v112, v112, 2, s10
	v_lshl_add_u32 v120, v120, 2, s10
	v_lshl_add_u32 v128, v128, 2, s10
	v_lshl_add_u32 v136, v136, 2, s10
	v_add_u32_e32 v114, 0x400, v34
	v_add_u32_e32 v122, 0x500, v34
	v_add_u32_e32 v130, 0x600, v34
	v_add_u32_e32 v138, 0x700, v34
	v_mov_b32_e32 v119, -1
	v_mov_b32_e32 v127, -1
	v_mov_b32_e32 v135, -1
	v_mov_b32_e32 v143, -1
	v_cmp_eq_u32_e32 vcc, v113, v2
	v_cmp_eq_u32_e64 s[0:1], v121, v2
	v_cmp_eq_u32_e64 s[6:7], v129, v2
	v_cmp_eq_u32_e64 s[8:9], v137, v2
	v_cndmask_b32_e32 v119, v119, v104, vcc
	v_cndmask_b32_e64 v127, v127, v104, s[0:1]
	v_cndmask_b32_e64 v135, v135, v104, s[6:7]
	v_cndmask_b32_e64 v143, v143, v104, s[8:9]
	v_cmp_eq_u32_e32 vcc, v113, v3
	v_cmp_eq_u32_e64 s[0:1], v121, v3
	v_cmp_eq_u32_e64 s[6:7], v129, v3
	v_cmp_eq_u32_e64 s[8:9], v137, v3
	v_cndmask_b32_e32 v119, v119, v105, vcc
	v_cndmask_b32_e64 v127, v127, v105, s[0:1]
	v_cndmask_b32_e64 v135, v135, v105, s[6:7]
	v_cndmask_b32_e64 v143, v143, v105, s[8:9]
	v_cmp_eq_u32_e32 vcc, v113, v4
	v_cmp_eq_u32_e64 s[0:1], v121, v4
	v_cmp_eq_u32_e64 s[6:7], v129, v4
	v_cmp_eq_u32_e64 s[8:9], v137, v4
	v_cndmask_b32_e32 v119, v119, v106, vcc
	v_cndmask_b32_e64 v127, v127, v106, s[0:1]
	v_cndmask_b32_e64 v135, v135, v106, s[6:7]
	v_cndmask_b32_e64 v143, v143, v106, s[8:9]
	v_cmp_eq_u32_e32 vcc, v113, v5
	v_cmp_eq_u32_e64 s[0:1], v121, v5
	v_cmp_eq_u32_e64 s[6:7], v129, v5
	v_cmp_eq_u32_e64 s[8:9], v137, v5
	v_cndmask_b32_e32 v119, v119, v107, vcc
	v_cndmask_b32_e64 v127, v127, v107, s[0:1]
	v_cndmask_b32_e64 v135, v135, v107, s[6:7]
	v_cndmask_b32_e64 v143, v143, v107, s[8:9]
	v_cmp_gt_i32_e32 vcc, 0, v6
	s_cbranch_vccnz .Lprep_a_m1
	v_cmp_eq_u32_e32 vcc, v113, v6
	v_cmp_eq_u32_e64 s[0:1], v121, v6
	v_cmp_eq_u32_e64 s[6:7], v129, v6
	v_cmp_eq_u32_e64 s[8:9], v137, v6
	v_cndmask_b32_e32 v119, v119, v108, vcc
	v_cndmask_b32_e64 v127, v127, v108, s[0:1]
	v_cndmask_b32_e64 v135, v135, v108, s[6:7]
	v_cndmask_b32_e64 v143, v143, v108, s[8:9]
	v_cmp_eq_u32_e32 vcc, v113, v7
	v_cmp_eq_u32_e64 s[0:1], v121, v7
	v_cmp_eq_u32_e64 s[6:7], v129, v7
	v_cmp_eq_u32_e64 s[8:9], v137, v7
	v_cndmask_b32_e32 v119, v119, v109, vcc
	v_cndmask_b32_e64 v127, v127, v109, s[0:1]
	v_cndmask_b32_e64 v135, v135, v109, s[6:7]
	v_cndmask_b32_e64 v143, v143, v109, s[8:9]
	v_cmp_eq_u32_e32 vcc, v113, v8
	v_cmp_eq_u32_e64 s[0:1], v121, v8
	v_cmp_eq_u32_e64 s[6:7], v129, v8
	v_cmp_eq_u32_e64 s[8:9], v137, v8
	v_cndmask_b32_e32 v119, v119, v110, vcc
	v_cndmask_b32_e64 v127, v127, v110, s[0:1]
	v_cndmask_b32_e64 v135, v135, v110, s[6:7]
	v_cndmask_b32_e64 v143, v143, v110, s[8:9]
	v_cmp_eq_u32_e32 vcc, v113, v9
	v_cmp_eq_u32_e64 s[0:1], v121, v9
	v_cmp_eq_u32_e64 s[6:7], v129, v9
	v_cmp_eq_u32_e64 s[8:9], v137, v9
	v_cndmask_b32_e32 v119, v119, v111, vcc
	v_cndmask_b32_e64 v127, v127, v111, s[0:1]
	v_cndmask_b32_e64 v135, v135, v111, s[6:7]
	v_cndmask_b32_e64 v143, v143, v111, s[8:9]
.Lprep_a_m1:
	v_add_u32_e32 v112, v112, v119
	v_add_u32_e32 v120, v120, v127
	v_add_u32_e32 v128, v128, v135
	v_add_u32_e32 v136, v136, v143
	v_cmp_ne_u32_e32 vcc, -1, v119
	s_and_saveexec_b64 s[24:25], vcc
	ds_write_b32 v112, v114
	s_mov_b64 exec, s[24:25]
	v_cmp_ne_u32_e32 vcc, -1, v127
	s_and_saveexec_b64 s[24:25], vcc
	ds_write_b32 v120, v122
	s_mov_b64 exec, s[24:25]
	v_cmp_ne_u32_e32 vcc, -1, v135
	s_and_saveexec_b64 s[24:25], vcc
	ds_write_b32 v128, v130
	s_mov_b64 exec, s[24:25]
	v_cmp_ne_u32_e32 vcc, -1, v143
	s_and_saveexec_b64 s[24:25], vcc
	ds_write_b32 v136, v138
	s_mov_b64 exec, s[24:25]
	v_and_b32_e32 v112, 0xff, v48
	v_and_b32_e32 v120, 0xff, v49
	v_and_b32_e32 v128, 0xff, v50
	v_and_b32_e32 v136, 0xff, v51
	v_lshlrev_b32_e32 v112, 2, v112
	v_lshlrev_b32_e32 v120, 2, v120
	v_lshlrev_b32_e32 v128, 2, v128
	v_lshlrev_b32_e32 v136, 2, v136
	v_add_u32_e32 v118, v112, v11
	v_add_u32_e32 v126, v120, v11
	v_add_u32_e32 v134, v128, v11
	v_add_u32_e32 v142, v136, v11
	ds_read_b32 v113, v112 offset:36864
	ds_read_b32 v114, v112 offset:35072
	ds_read_b32 v115, v118 offset:4096
	ds_read_b32 v121, v120 offset:36864
	ds_read_b32 v122, v120 offset:35072
	ds_read_b32 v123, v126 offset:4608
	ds_read_b32 v129, v128 offset:36864
	ds_read_b32 v130, v128 offset:35072
	ds_read_b32 v131, v134 offset:5120
	ds_read_b32 v137, v136 offset:36864
	ds_read_b32 v138, v136 offset:35072
	ds_read_b32 v139, v142 offset:5632
	v_mov_b32_e32 v117, v37
	v_add_u32_e32 v37, 4, v37
	v_subrev_u32_e32 v118, s11, v37
	v_min_u32_e32 v37, v37, v118
	v_subrev_u32_e32 v118, s11, v37
	v_min_u32_e32 v37, v37, v118
	v_mov_b32_e32 v125, v37
	v_add_u32_e32 v37, 4, v37
	v_subrev_u32_e32 v126, s11, v37
	v_min_u32_e32 v37, v37, v126
	v_subrev_u32_e32 v126, s11, v37
	v_min_u32_e32 v37, v37, v126
	v_mov_b32_e32 v133, v37
	v_add_u32_e32 v37, 4, v37
	v_subrev_u32_e32 v134, s11, v37
	v_min_u32_e32 v37, v37, v134
	v_subrev_u32_e32 v134, s11, v37
	v_min_u32_e32 v37, v37, v134
	v_mov_b32_e32 v141, v37
	v_add_u32_e32 v37, 4, v37
	v_subrev_u32_e32 v142, s11, v37
	v_min_u32_e32 v37, v37, v142
	v_subrev_u32_e32 v142, s11, v37
	v_min_u32_e32 v37, v37, v142
	v_ashrrev_i32_e32 v116, 8, v48
	v_ashrrev_i32_e32 v124, 8, v49
	v_ashrrev_i32_e32 v132, 8, v50
	v_ashrrev_i32_e32 v140, 8, v51
	s_waitcnt lgkmcnt(0)
	v_add_u32_e32 v116, v116, v113
	v_add_u32_e32 v124, v124, v121
	v_add_u32_e32 v132, v132, v129
	v_add_u32_e32 v140, v140, v137
	v_add3_u32 v116, v116, v114, v115
	v_add3_u32 v124, v124, v122, v123
	v_add3_u32 v132, v132, v130, v131
	v_add3_u32 v140, v140, v138, v139
	v_cmp_eq_u32_e32 vcc, s93, v117
	v_add_u32_e32 v1, 0x4000, v10
	s_and_saveexec_b64 s[24:25], vcc
	global_store_dword v1, v116, s[16:17]
	s_mov_b64 exec, s[24:25]
	v_cmp_eq_u32_e32 vcc, s93, v125
	v_add_u32_e32 v1, 0x4800, v10
	s_and_saveexec_b64 s[24:25], vcc
	global_store_dword v1, v124, s[16:17]
	s_mov_b64 exec, s[24:25]
	v_cmp_eq_u32_e32 vcc, s93, v133
	v_add_u32_e32 v1, 0x5000, v10
	s_and_saveexec_b64 s[24:25], vcc
	global_store_dword v1, v132, s[16:17]
	s_mov_b64 exec, s[24:25]
	v_cmp_eq_u32_e32 vcc, s93, v141
	v_add_u32_e32 v1, 0x5800, v10
	s_and_saveexec_b64 s[24:25], vcc
	global_store_dword v1, v140, s[16:17]
	s_mov_b64 exec, s[24:25]
	v_ashrrev_i32_e32 v113, 8, v116
	v_ashrrev_i32_e32 v121, 8, v124
	v_ashrrev_i32_e32 v129, 8, v132
	v_ashrrev_i32_e32 v137, 8, v140
	v_and_b32_e32 v112, 0xff, v116
	v_and_b32_e32 v120, 0xff, v124
	v_and_b32_e32 v128, 0xff, v132
	v_and_b32_e32 v136, 0xff, v140
	v_lshl_add_u32 v112, v112, 2, s10
	v_lshl_add_u32 v120, v120, 2, s10
	v_lshl_add_u32 v128, v128, 2, s10
	v_lshl_add_u32 v136, v136, 2, s10
	v_add_u32_e32 v114, 0x800, v34
	v_add_u32_e32 v122, 0x900, v34
	v_add_u32_e32 v130, 0xa00, v34
	v_add_u32_e32 v138, 0xb00, v34
	v_mov_b32_e32 v119, -1
	v_mov_b32_e32 v127, -1
	v_mov_b32_e32 v135, -1
	v_mov_b32_e32 v143, -1
	v_cmp_eq_u32_e32 vcc, v113, v2
	v_cmp_eq_u32_e64 s[0:1], v121, v2
	v_cmp_eq_u32_e64 s[6:7], v129, v2
	v_cmp_eq_u32_e64 s[8:9], v137, v2
	v_cndmask_b32_e32 v119, v119, v104, vcc
	v_cndmask_b32_e64 v127, v127, v104, s[0:1]
	v_cndmask_b32_e64 v135, v135, v104, s[6:7]
	v_cndmask_b32_e64 v143, v143, v104, s[8:9]
	v_cmp_eq_u32_e32 vcc, v113, v3
	v_cmp_eq_u32_e64 s[0:1], v121, v3
	v_cmp_eq_u32_e64 s[6:7], v129, v3
	v_cmp_eq_u32_e64 s[8:9], v137, v3
	v_cndmask_b32_e32 v119, v119, v105, vcc
	v_cndmask_b32_e64 v127, v127, v105, s[0:1]
	v_cndmask_b32_e64 v135, v135, v105, s[6:7]
	v_cndmask_b32_e64 v143, v143, v105, s[8:9]
	v_cmp_eq_u32_e32 vcc, v113, v4
	v_cmp_eq_u32_e64 s[0:1], v121, v4
	v_cmp_eq_u32_e64 s[6:7], v129, v4
	v_cmp_eq_u32_e64 s[8:9], v137, v4
	v_cndmask_b32_e32 v119, v119, v106, vcc
	v_cndmask_b32_e64 v127, v127, v106, s[0:1]
	v_cndmask_b32_e64 v135, v135, v106, s[6:7]
	v_cndmask_b32_e64 v143, v143, v106, s[8:9]
	v_cmp_eq_u32_e32 vcc, v113, v5
	v_cmp_eq_u32_e64 s[0:1], v121, v5
	v_cmp_eq_u32_e64 s[6:7], v129, v5
	v_cmp_eq_u32_e64 s[8:9], v137, v5
	v_cndmask_b32_e32 v119, v119, v107, vcc
	v_cndmask_b32_e64 v127, v127, v107, s[0:1]
	v_cndmask_b32_e64 v135, v135, v107, s[6:7]
	v_cndmask_b32_e64 v143, v143, v107, s[8:9]
	v_cmp_gt_i32_e32 vcc, 0, v6
	s_cbranch_vccnz .Lprep_a_m2
	v_cmp_eq_u32_e32 vcc, v113, v6
	v_cmp_eq_u32_e64 s[0:1], v121, v6
	v_cmp_eq_u32_e64 s[6:7], v129, v6
	v_cmp_eq_u32_e64 s[8:9], v137, v6
	v_cndmask_b32_e32 v119, v119, v108, vcc
	v_cndmask_b32_e64 v127, v127, v108, s[0:1]
	v_cndmask_b32_e64 v135, v135, v108, s[6:7]
	v_cndmask_b32_e64 v143, v143, v108, s[8:9]
	v_cmp_eq_u32_e32 vcc, v113, v7
	v_cmp_eq_u32_e64 s[0:1], v121, v7
	v_cmp_eq_u32_e64 s[6:7], v129, v7
	v_cmp_eq_u32_e64 s[8:9], v137, v7
	v_cndmask_b32_e32 v119, v119, v109, vcc
	v_cndmask_b32_e64 v127, v127, v109, s[0:1]
	v_cndmask_b32_e64 v135, v135, v109, s[6:7]
	v_cndmask_b32_e64 v143, v143, v109, s[8:9]
	v_cmp_eq_u32_e32 vcc, v113, v8
	v_cmp_eq_u32_e64 s[0:1], v121, v8
	v_cmp_eq_u32_e64 s[6:7], v129, v8
	v_cmp_eq_u32_e64 s[8:9], v137, v8
	v_cndmask_b32_e32 v119, v119, v110, vcc
	v_cndmask_b32_e64 v127, v127, v110, s[0:1]
	v_cndmask_b32_e64 v135, v135, v110, s[6:7]
	v_cndmask_b32_e64 v143, v143, v110, s[8:9]
	v_cmp_eq_u32_e32 vcc, v113, v9
	v_cmp_eq_u32_e64 s[0:1], v121, v9
	v_cmp_eq_u32_e64 s[6:7], v129, v9
	v_cmp_eq_u32_e64 s[8:9], v137, v9
	v_cndmask_b32_e32 v119, v119, v111, vcc
	v_cndmask_b32_e64 v127, v127, v111, s[0:1]
	v_cndmask_b32_e64 v135, v135, v111, s[6:7]
	v_cndmask_b32_e64 v143, v143, v111, s[8:9]
.Lprep_a_m2:
	v_add_u32_e32 v112, v112, v119
	v_add_u32_e32 v120, v120, v127
	v_add_u32_e32 v128, v128, v135
	v_add_u32_e32 v136, v136, v143
	v_cmp_ne_u32_e32 vcc, -1, v119
	s_and_saveexec_b64 s[24:25], vcc
	ds_write_b32 v112, v114
	s_mov_b64 exec, s[24:25]
	v_cmp_ne_u32_e32 vcc, -1, v127
	s_and_saveexec_b64 s[24:25], vcc
	ds_write_b32 v120, v122
	s_mov_b64 exec, s[24:25]
	v_cmp_ne_u32_e32 vcc, -1, v135
	s_and_saveexec_b64 s[24:25], vcc
	ds_write_b32 v128, v130
	s_mov_b64 exec, s[24:25]
	v_cmp_ne_u32_e32 vcc, -1, v143
	s_and_saveexec_b64 s[24:25], vcc
	ds_write_b32 v136, v138
	s_mov_b64 exec, s[24:25]
	v_and_b32_e32 v112, 0xff, v52
	v_and_b32_e32 v120, 0xff, v53
	v_and_b32_e32 v128, 0xff, v54
	v_and_b32_e32 v136, 0xff, v55
	v_lshlrev_b32_e32 v112, 2, v112
	v_lshlrev_b32_e32 v120, 2, v120
	v_lshlrev_b32_e32 v128, 2, v128
	v_lshlrev_b32_e32 v136, 2, v136
	v_add_u32_e32 v118, v112, v11
	v_add_u32_e32 v126, v120, v11
	v_add_u32_e32 v134, v128, v11
	v_add_u32_e32 v142, v136, v11
	ds_read_b32 v113, v112 offset:36864
	ds_read_b32 v114, v112 offset:35200
	ds_read_b32 v115, v118 offset:6144
	ds_read_b32 v121, v120 offset:36864
	ds_read_b32 v122, v120 offset:35200
	ds_read_b32 v123, v126 offset:6656
	ds_read_b32 v129, v128 offset:36864
	ds_read_b32 v130, v128 offset:35200
	ds_read_b32 v131, v134 offset:7168
	ds_read_b32 v137, v136 offset:36864
	ds_read_b32 v138, v136 offset:35200
	ds_read_b32 v139, v142 offset:7680
	v_mov_b32_e32 v117, v37
	v_add_u32_e32 v37, 4, v37
	v_subrev_u32_e32 v118, s11, v37
	v_min_u32_e32 v37, v37, v118
	v_subrev_u32_e32 v118, s11, v37
	v_min_u32_e32 v37, v37, v118
	v_mov_b32_e32 v125, v37
	v_add_u32_e32 v37, 4, v37
	v_subrev_u32_e32 v126, s11, v37
	v_min_u32_e32 v37, v37, v126
	v_subrev_u32_e32 v126, s11, v37
	v_min_u32_e32 v37, v37, v126
	v_mov_b32_e32 v133, v37
	v_add_u32_e32 v37, 4, v37
	v_subrev_u32_e32 v134, s11, v37
	v_min_u32_e32 v37, v37, v134
	v_subrev_u32_e32 v134, s11, v37
	v_min_u32_e32 v37, v37, v134
	v_mov_b32_e32 v141, v37
	v_add_u32_e32 v37, 4, v37
	v_subrev_u32_e32 v142, s11, v37
	v_min_u32_e32 v37, v37, v142
	v_subrev_u32_e32 v142, s11, v37
	v_min_u32_e32 v37, v37, v142
	v_ashrrev_i32_e32 v116, 8, v52
	v_ashrrev_i32_e32 v124, 8, v53
	v_ashrrev_i32_e32 v132, 8, v54
	v_ashrrev_i32_e32 v140, 8, v55
	s_waitcnt lgkmcnt(0)
	v_add_u32_e32 v116, v116, v113
	v_add_u32_e32 v124, v124, v121
	v_add_u32_e32 v132, v132, v129
	v_add_u32_e32 v140, v140, v137
	v_add3_u32 v116, v116, v114, v115
	v_add3_u32 v124, v124, v122, v123
	v_add3_u32 v132, v132, v130, v131
	v_add3_u32 v140, v140, v138, v139
	v_cmp_eq_u32_e32 vcc, s93, v117
	v_add_u32_e32 v1, 0x6000, v10
	s_and_saveexec_b64 s[24:25], vcc
	global_store_dword v1, v116, s[16:17]
	s_mov_b64 exec, s[24:25]
	v_cmp_eq_u32_e32 vcc, s93, v125
	v_add_u32_e32 v1, 0x6800, v10
	s_and_saveexec_b64 s[24:25], vcc
	global_store_dword v1, v124, s[16:17]
	s_mov_b64 exec, s[24:25]
	v_cmp_eq_u32_e32 vcc, s93, v133
	v_add_u32_e32 v1, 0x7000, v10
	s_and_saveexec_b64 s[24:25], vcc
	global_store_dword v1, v132, s[16:17]
	s_mov_b64 exec, s[24:25]
	v_cmp_eq_u32_e32 vcc, s93, v141
	v_add_u32_e32 v1, 0x7800, v10
	s_and_saveexec_b64 s[24:25], vcc
	global_store_dword v1, v140, s[16:17]
	s_mov_b64 exec, s[24:25]
	v_ashrrev_i32_e32 v113, 8, v116
	v_ashrrev_i32_e32 v121, 8, v124
	v_ashrrev_i32_e32 v129, 8, v132
	v_ashrrev_i32_e32 v137, 8, v140
	v_and_b32_e32 v112, 0xff, v116
	v_and_b32_e32 v120, 0xff, v124
	v_and_b32_e32 v128, 0xff, v132
	v_and_b32_e32 v136, 0xff, v140
	v_lshl_add_u32 v112, v112, 2, s10
	v_lshl_add_u32 v120, v120, 2, s10
	v_lshl_add_u32 v128, v128, 2, s10
	v_lshl_add_u32 v136, v136, 2, s10
	v_add_u32_e32 v114, 0xc00, v34
	v_add_u32_e32 v122, 0xd00, v34
	v_add_u32_e32 v130, 0xe00, v34
	v_add_u32_e32 v138, 0xf00, v34
	v_mov_b32_e32 v119, -1
	v_mov_b32_e32 v127, -1
	v_mov_b32_e32 v135, -1
	v_mov_b32_e32 v143, -1
	v_cmp_eq_u32_e32 vcc, v113, v2
	v_cmp_eq_u32_e64 s[0:1], v121, v2
	v_cmp_eq_u32_e64 s[6:7], v129, v2
	v_cmp_eq_u32_e64 s[8:9], v137, v2
	v_cndmask_b32_e32 v119, v119, v104, vcc
	v_cndmask_b32_e64 v127, v127, v104, s[0:1]
	v_cndmask_b32_e64 v135, v135, v104, s[6:7]
	v_cndmask_b32_e64 v143, v143, v104, s[8:9]
	v_cmp_eq_u32_e32 vcc, v113, v3
	v_cmp_eq_u32_e64 s[0:1], v121, v3
	v_cmp_eq_u32_e64 s[6:7], v129, v3
	v_cmp_eq_u32_e64 s[8:9], v137, v3
	v_cndmask_b32_e32 v119, v119, v105, vcc
	v_cndmask_b32_e64 v127, v127, v105, s[0:1]
	v_cndmask_b32_e64 v135, v135, v105, s[6:7]
	v_cndmask_b32_e64 v143, v143, v105, s[8:9]
	v_cmp_eq_u32_e32 vcc, v113, v4
	v_cmp_eq_u32_e64 s[0:1], v121, v4
	v_cmp_eq_u32_e64 s[6:7], v129, v4
	v_cmp_eq_u32_e64 s[8:9], v137, v4
	v_cndmask_b32_e32 v119, v119, v106, vcc
	v_cndmask_b32_e64 v127, v127, v106, s[0:1]
	v_cndmask_b32_e64 v135, v135, v106, s[6:7]
	v_cndmask_b32_e64 v143, v143, v106, s[8:9]
	v_cmp_eq_u32_e32 vcc, v113, v5
	v_cmp_eq_u32_e64 s[0:1], v121, v5
	v_cmp_eq_u32_e64 s[6:7], v129, v5
	v_cmp_eq_u32_e64 s[8:9], v137, v5
	v_cndmask_b32_e32 v119, v119, v107, vcc
	v_cndmask_b32_e64 v127, v127, v107, s[0:1]
	v_cndmask_b32_e64 v135, v135, v107, s[6:7]
	v_cndmask_b32_e64 v143, v143, v107, s[8:9]
	v_cmp_gt_i32_e32 vcc, 0, v6
	s_cbranch_vccnz .Lprep_a_m3
	v_cmp_eq_u32_e32 vcc, v113, v6
	v_cmp_eq_u32_e64 s[0:1], v121, v6
	v_cmp_eq_u32_e64 s[6:7], v129, v6
	v_cmp_eq_u32_e64 s[8:9], v137, v6
	v_cndmask_b32_e32 v119, v119, v108, vcc
	v_cndmask_b32_e64 v127, v127, v108, s[0:1]
	v_cndmask_b32_e64 v135, v135, v108, s[6:7]
	v_cndmask_b32_e64 v143, v143, v108, s[8:9]
	v_cmp_eq_u32_e32 vcc, v113, v7
	v_cmp_eq_u32_e64 s[0:1], v121, v7
	v_cmp_eq_u32_e64 s[6:7], v129, v7
	v_cmp_eq_u32_e64 s[8:9], v137, v7
	v_cndmask_b32_e32 v119, v119, v109, vcc
	v_cndmask_b32_e64 v127, v127, v109, s[0:1]
	v_cndmask_b32_e64 v135, v135, v109, s[6:7]
	v_cndmask_b32_e64 v143, v143, v109, s[8:9]
	v_cmp_eq_u32_e32 vcc, v113, v8
	v_cmp_eq_u32_e64 s[0:1], v121, v8
	v_cmp_eq_u32_e64 s[6:7], v129, v8
	v_cmp_eq_u32_e64 s[8:9], v137, v8
	v_cndmask_b32_e32 v119, v119, v110, vcc
	v_cndmask_b32_e64 v127, v127, v110, s[0:1]
	v_cndmask_b32_e64 v135, v135, v110, s[6:7]
	v_cndmask_b32_e64 v143, v143, v110, s[8:9]
	v_cmp_eq_u32_e32 vcc, v113, v9
	v_cmp_eq_u32_e64 s[0:1], v121, v9
	v_cmp_eq_u32_e64 s[6:7], v129, v9
	v_cmp_eq_u32_e64 s[8:9], v137, v9
	v_cndmask_b32_e32 v119, v119, v111, vcc
	v_cndmask_b32_e64 v127, v127, v111, s[0:1]
	v_cndmask_b32_e64 v135, v135, v111, s[6:7]
	v_cndmask_b32_e64 v143, v143, v111, s[8:9]
.Lprep_a_m3:
	v_add_u32_e32 v112, v112, v119
	v_add_u32_e32 v120, v120, v127
	v_add_u32_e32 v128, v128, v135
	v_add_u32_e32 v136, v136, v143
	v_cmp_ne_u32_e32 vcc, -1, v119
	s_and_saveexec_b64 s[24:25], vcc
	ds_write_b32 v112, v114
	s_mov_b64 exec, s[24:25]
	v_cmp_ne_u32_e32 vcc, -1, v127
	s_and_saveexec_b64 s[24:25], vcc
	ds_write_b32 v120, v122
	s_mov_b64 exec, s[24:25]
	v_cmp_ne_u32_e32 vcc, -1, v135
	s_and_saveexec_b64 s[24:25], vcc
	ds_write_b32 v128, v130
	s_mov_b64 exec, s[24:25]
	v_cmp_ne_u32_e32 vcc, -1, v143
	s_and_saveexec_b64 s[24:25], vcc
	ds_write_b32 v136, v138
	s_mov_b64 exec, s[24:25]
	v_and_b32_e32 v112, 0xff, v56
	v_and_b32_e32 v120, 0xff, v57
	v_and_b32_e32 v128, 0xff, v58
	v_and_b32_e32 v136, 0xff, v59
	v_lshlrev_b32_e32 v112, 2, v112
	v_lshlrev_b32_e32 v120, 2, v120
	v_lshlrev_b32_e32 v128, 2, v128
	v_lshlrev_b32_e32 v136, 2, v136
	v_add_u32_e32 v118, v112, v11
	v_add_u32_e32 v126, v120, v11
	v_add_u32_e32 v134, v128, v11
	v_add_u32_e32 v142, v136, v11
	ds_read_b32 v113, v112 offset:36864
	ds_read_b32 v114, v112 offset:35328
	ds_read_b32 v115, v118 offset:8192
	ds_read_b32 v121, v120 offset:36864
	ds_read_b32 v122, v120 offset:35328
	ds_read_b32 v123, v126 offset:8704
	ds_read_b32 v129, v128 offset:36864
	ds_read_b32 v130, v128 offset:35328
	ds_read_b32 v131, v134 offset:9216
	ds_read_b32 v137, v136 offset:36864
	ds_read_b32 v138, v136 offset:35328
	ds_read_b32 v139, v142 offset:9728
	v_mov_b32_e32 v117, v37
	v_add_u32_e32 v37, 4, v37
	v_subrev_u32_e32 v118, s11, v37
	v_min_u32_e32 v37, v37, v118
	v_subrev_u32_e32 v118, s11, v37
	v_min_u32_e32 v37, v37, v118
	v_mov_b32_e32 v125, v37
	v_add_u32_e32 v37, 4, v37
	v_subrev_u32_e32 v126, s11, v37
	v_min_u32_e32 v37, v37, v126
	v_subrev_u32_e32 v126, s11, v37
	v_min_u32_e32 v37, v37, v126
	v_mov_b32_e32 v133, v37
	v_add_u32_e32 v37, 4, v37
	v_subrev_u32_e32 v134, s11, v37
	v_min_u32_e32 v37, v37, v134
	v_subrev_u32_e32 v134, s11, v37
	v_min_u32_e32 v37, v37, v134
	v_mov_b32_e32 v141, v37
	v_add_u32_e32 v37, 4, v37
	v_subrev_u32_e32 v142, s11, v37
	v_min_u32_e32 v37, v37, v142
	v_subrev_u32_e32 v142, s11, v37
	v_min_u32_e32 v37, v37, v142
	v_ashrrev_i32_e32 v116, 8, v56
	v_ashrrev_i32_e32 v124, 8, v57
	v_ashrrev_i32_e32 v132, 8, v58
	v_ashrrev_i32_e32 v140, 8, v59
	s_waitcnt lgkmcnt(0)
	v_add_u32_e32 v116, v116, v113
	v_add_u32_e32 v124, v124, v121
	v_add_u32_e32 v132, v132, v129
	v_add_u32_e32 v140, v140, v137
	v_add3_u32 v116, v116, v114, v115
	v_add3_u32 v124, v124, v122, v123
	v_add3_u32 v132, v132, v130, v131
	v_add3_u32 v140, v140, v138, v139
	v_cmp_eq_u32_e32 vcc, s93, v117
	v_add_u32_e32 v1, 0x8000, v10
	s_and_saveexec_b64 s[24:25], vcc
	global_store_dword v1, v116, s[16:17]
	s_mov_b64 exec, s[24:25]
	v_cmp_eq_u32_e32 vcc, s93, v125
	v_add_u32_e32 v1, 0x8800, v10
	s_and_saveexec_b64 s[24:25], vcc
	global_store_dword v1, v124, s[16:17]
	s_mov_b64 exec, s[24:25]
	v_cmp_eq_u32_e32 vcc, s93, v133
	v_add_u32_e32 v1, 0x9000, v10
	s_and_saveexec_b64 s[24:25], vcc
	global_store_dword v1, v132, s[16:17]
	s_mov_b64 exec, s[24:25]
	v_cmp_eq_u32_e32 vcc, s93, v141
	v_add_u32_e32 v1, 0x9800, v10
	s_and_saveexec_b64 s[24:25], vcc
	global_store_dword v1, v140, s[16:17]
	s_mov_b64 exec, s[24:25]
	v_ashrrev_i32_e32 v113, 8, v116
	v_ashrrev_i32_e32 v121, 8, v124
	v_ashrrev_i32_e32 v129, 8, v132
	v_ashrrev_i32_e32 v137, 8, v140
	v_and_b32_e32 v112, 0xff, v116
	v_and_b32_e32 v120, 0xff, v124
	v_and_b32_e32 v128, 0xff, v132
	v_and_b32_e32 v136, 0xff, v140
	v_lshl_add_u32 v112, v112, 2, s10
	v_lshl_add_u32 v120, v120, 2, s10
	v_lshl_add_u32 v128, v128, 2, s10
	v_lshl_add_u32 v136, v136, 2, s10
	v_add_u32_e32 v114, 0x1000, v34
	v_add_u32_e32 v122, 0x1100, v34
	v_add_u32_e32 v130, 0x1200, v34
	v_add_u32_e32 v138, 0x1300, v34
	v_mov_b32_e32 v119, -1
	v_mov_b32_e32 v127, -1
	v_mov_b32_e32 v135, -1
	v_mov_b32_e32 v143, -1
	v_cmp_eq_u32_e32 vcc, v113, v2
	v_cmp_eq_u32_e64 s[0:1], v121, v2
	v_cmp_eq_u32_e64 s[6:7], v129, v2
	v_cmp_eq_u32_e64 s[8:9], v137, v2
	v_cndmask_b32_e32 v119, v119, v104, vcc
	v_cndmask_b32_e64 v127, v127, v104, s[0:1]
	v_cndmask_b32_e64 v135, v135, v104, s[6:7]
	v_cndmask_b32_e64 v143, v143, v104, s[8:9]
	v_cmp_eq_u32_e32 vcc, v113, v3
	v_cmp_eq_u32_e64 s[0:1], v121, v3
	v_cmp_eq_u32_e64 s[6:7], v129, v3
	v_cmp_eq_u32_e64 s[8:9], v137, v3
	v_cndmask_b32_e32 v119, v119, v105, vcc
	v_cndmask_b32_e64 v127, v127, v105, s[0:1]
	v_cndmask_b32_e64 v135, v135, v105, s[6:7]
	v_cndmask_b32_e64 v143, v143, v105, s[8:9]
	v_cmp_eq_u32_e32 vcc, v113, v4
	v_cmp_eq_u32_e64 s[0:1], v121, v4
	v_cmp_eq_u32_e64 s[6:7], v129, v4
	v_cmp_eq_u32_e64 s[8:9], v137, v4
	v_cndmask_b32_e32 v119, v119, v106, vcc
	v_cndmask_b32_e64 v127, v127, v106, s[0:1]
	v_cndmask_b32_e64 v135, v135, v106, s[6:7]
	v_cndmask_b32_e64 v143, v143, v106, s[8:9]
	v_cmp_eq_u32_e32 vcc, v113, v5
	v_cmp_eq_u32_e64 s[0:1], v121, v5
	v_cmp_eq_u32_e64 s[6:7], v129, v5
	v_cmp_eq_u32_e64 s[8:9], v137, v5
	v_cndmask_b32_e32 v119, v119, v107, vcc
	v_cndmask_b32_e64 v127, v127, v107, s[0:1]
	v_cndmask_b32_e64 v135, v135, v107, s[6:7]
	v_cndmask_b32_e64 v143, v143, v107, s[8:9]
	v_cmp_gt_i32_e32 vcc, 0, v6
	s_cbranch_vccnz .Lprep_a_m4
	v_cmp_eq_u32_e32 vcc, v113, v6
	v_cmp_eq_u32_e64 s[0:1], v121, v6
	v_cmp_eq_u32_e64 s[6:7], v129, v6
	v_cmp_eq_u32_e64 s[8:9], v137, v6
	v_cndmask_b32_e32 v119, v119, v108, vcc
	v_cndmask_b32_e64 v127, v127, v108, s[0:1]
	v_cndmask_b32_e64 v135, v135, v108, s[6:7]
	v_cndmask_b32_e64 v143, v143, v108, s[8:9]
	v_cmp_eq_u32_e32 vcc, v113, v7
	v_cmp_eq_u32_e64 s[0:1], v121, v7
	v_cmp_eq_u32_e64 s[6:7], v129, v7
	v_cmp_eq_u32_e64 s[8:9], v137, v7
	v_cndmask_b32_e32 v119, v119, v109, vcc
	v_cndmask_b32_e64 v127, v127, v109, s[0:1]
	v_cndmask_b32_e64 v135, v135, v109, s[6:7]
	v_cndmask_b32_e64 v143, v143, v109, s[8:9]
	v_cmp_eq_u32_e32 vcc, v113, v8
	v_cmp_eq_u32_e64 s[0:1], v121, v8
	v_cmp_eq_u32_e64 s[6:7], v129, v8
	v_cmp_eq_u32_e64 s[8:9], v137, v8
	v_cndmask_b32_e32 v119, v119, v110, vcc
	v_cndmask_b32_e64 v127, v127, v110, s[0:1]
	v_cndmask_b32_e64 v135, v135, v110, s[6:7]
	v_cndmask_b32_e64 v143, v143, v110, s[8:9]
	v_cmp_eq_u32_e32 vcc, v113, v9
	v_cmp_eq_u32_e64 s[0:1], v121, v9
	v_cmp_eq_u32_e64 s[6:7], v129, v9
	v_cmp_eq_u32_e64 s[8:9], v137, v9
	v_cndmask_b32_e32 v119, v119, v111, vcc
	v_cndmask_b32_e64 v127, v127, v111, s[0:1]
	v_cndmask_b32_e64 v135, v135, v111, s[6:7]
	v_cndmask_b32_e64 v143, v143, v111, s[8:9]
.Lprep_a_m4:
	v_add_u32_e32 v112, v112, v119
	v_add_u32_e32 v120, v120, v127
	v_add_u32_e32 v128, v128, v135
	v_add_u32_e32 v136, v136, v143
	v_cmp_ne_u32_e32 vcc, -1, v119
	s_and_saveexec_b64 s[24:25], vcc
	ds_write_b32 v112, v114
	s_mov_b64 exec, s[24:25]
	v_cmp_ne_u32_e32 vcc, -1, v127
	s_and_saveexec_b64 s[24:25], vcc
	ds_write_b32 v120, v122
	s_mov_b64 exec, s[24:25]
	v_cmp_ne_u32_e32 vcc, -1, v135
	s_and_saveexec_b64 s[24:25], vcc
	ds_write_b32 v128, v130
	s_mov_b64 exec, s[24:25]
	v_cmp_ne_u32_e32 vcc, -1, v143
	s_and_saveexec_b64 s[24:25], vcc
	ds_write_b32 v136, v138
	s_mov_b64 exec, s[24:25]
	v_and_b32_e32 v112, 0xff, v60
	v_and_b32_e32 v120, 0xff, v61
	v_and_b32_e32 v128, 0xff, v62
	v_and_b32_e32 v136, 0xff, v63
	v_lshlrev_b32_e32 v112, 2, v112
	v_lshlrev_b32_e32 v120, 2, v120
	v_lshlrev_b32_e32 v128, 2, v128
	v_lshlrev_b32_e32 v136, 2, v136
	v_add_u32_e32 v118, v112, v11
	v_add_u32_e32 v126, v120, v11
	v_add_u32_e32 v134, v128, v11
	v_add_u32_e32 v142, v136, v11
	ds_read_b32 v113, v112 offset:36864
	ds_read_b32 v114, v112 offset:35456
	ds_read_b32 v115, v118 offset:10240
	ds_read_b32 v121, v120 offset:36864
	ds_read_b32 v122, v120 offset:35456
	ds_read_b32 v123, v126 offset:10752
	ds_read_b32 v129, v128 offset:36864
	ds_read_b32 v130, v128 offset:35456
	ds_read_b32 v131, v134 offset:11264
	ds_read_b32 v137, v136 offset:36864
	ds_read_b32 v138, v136 offset:35456
	ds_read_b32 v139, v142 offset:11776
	v_mov_b32_e32 v117, v37
	v_add_u32_e32 v37, 4, v37
	v_subrev_u32_e32 v118, s11, v37
	v_min_u32_e32 v37, v37, v118
	v_subrev_u32_e32 v118, s11, v37
	v_min_u32_e32 v37, v37, v118
	v_mov_b32_e32 v125, v37
	v_add_u32_e32 v37, 4, v37
	v_subrev_u32_e32 v126, s11, v37
	v_min_u32_e32 v37, v37, v126
	v_subrev_u32_e32 v126, s11, v37
	v_min_u32_e32 v37, v37, v126
	v_mov_b32_e32 v133, v37
	v_add_u32_e32 v37, 4, v37
	v_subrev_u32_e32 v134, s11, v37
	v_min_u32_e32 v37, v37, v134
	v_subrev_u32_e32 v134, s11, v37
	v_min_u32_e32 v37, v37, v134
	v_mov_b32_e32 v141, v37
	v_add_u32_e32 v37, 4, v37
	v_subrev_u32_e32 v142, s11, v37
	v_min_u32_e32 v37, v37, v142
	v_subrev_u32_e32 v142, s11, v37
	v_min_u32_e32 v37, v37, v142
	v_ashrrev_i32_e32 v116, 8, v60
	v_ashrrev_i32_e32 v124, 8, v61
	v_ashrrev_i32_e32 v132, 8, v62
	v_ashrrev_i32_e32 v140, 8, v63
	s_waitcnt lgkmcnt(0)
	v_add_u32_e32 v116, v116, v113
	v_add_u32_e32 v124, v124, v121
	v_add_u32_e32 v132, v132, v129
	v_add_u32_e32 v140, v140, v137
	v_add3_u32 v116, v116, v114, v115
	v_add3_u32 v124, v124, v122, v123
	v_add3_u32 v132, v132, v130, v131
	v_add3_u32 v140, v140, v138, v139
	v_cmp_eq_u32_e32 vcc, s93, v117
	v_add_u32_e32 v1, 0xa000, v10
	s_and_saveexec_b64 s[24:25], vcc
	global_store_dword v1, v116, s[16:17]
	s_mov_b64 exec, s[24:25]
	v_cmp_eq_u32_e32 vcc, s93, v125
	v_add_u32_e32 v1, 0xa800, v10
	s_and_saveexec_b64 s[24:25], vcc
	global_store_dword v1, v124, s[16:17]
	s_mov_b64 exec, s[24:25]
	v_cmp_eq_u32_e32 vcc, s93, v133
	v_add_u32_e32 v1, 0xb000, v10
	s_and_saveexec_b64 s[24:25], vcc
	global_store_dword v1, v132, s[16:17]
	s_mov_b64 exec, s[24:25]
	v_cmp_eq_u32_e32 vcc, s93, v141
	v_add_u32_e32 v1, 0xb800, v10
	s_and_saveexec_b64 s[24:25], vcc
	global_store_dword v1, v140, s[16:17]
	s_mov_b64 exec, s[24:25]
	v_ashrrev_i32_e32 v113, 8, v116
	v_ashrrev_i32_e32 v121, 8, v124
	v_ashrrev_i32_e32 v129, 8, v132
	v_ashrrev_i32_e32 v137, 8, v140
	v_and_b32_e32 v112, 0xff, v116
	v_and_b32_e32 v120, 0xff, v124
	v_and_b32_e32 v128, 0xff, v132
	v_and_b32_e32 v136, 0xff, v140
	v_lshl_add_u32 v112, v112, 2, s10
	v_lshl_add_u32 v120, v120, 2, s10
	v_lshl_add_u32 v128, v128, 2, s10
	v_lshl_add_u32 v136, v136, 2, s10
	v_add_u32_e32 v114, 0x1400, v34
	v_add_u32_e32 v122, 0x1500, v34
	v_add_u32_e32 v130, 0x1600, v34
	v_add_u32_e32 v138, 0x1700, v34
	v_mov_b32_e32 v119, -1
	v_mov_b32_e32 v127, -1
	v_mov_b32_e32 v135, -1
	v_mov_b32_e32 v143, -1
	v_cmp_eq_u32_e32 vcc, v113, v2
	v_cmp_eq_u32_e64 s[0:1], v121, v2
	v_cmp_eq_u32_e64 s[6:7], v129, v2
	v_cmp_eq_u32_e64 s[8:9], v137, v2
	v_cndmask_b32_e32 v119, v119, v104, vcc
	v_cndmask_b32_e64 v127, v127, v104, s[0:1]
	v_cndmask_b32_e64 v135, v135, v104, s[6:7]
	v_cndmask_b32_e64 v143, v143, v104, s[8:9]
	v_cmp_eq_u32_e32 vcc, v113, v3
	v_cmp_eq_u32_e64 s[0:1], v121, v3
	v_cmp_eq_u32_e64 s[6:7], v129, v3
	v_cmp_eq_u32_e64 s[8:9], v137, v3
	v_cndmask_b32_e32 v119, v119, v105, vcc
	v_cndmask_b32_e64 v127, v127, v105, s[0:1]
	v_cndmask_b32_e64 v135, v135, v105, s[6:7]
	v_cndmask_b32_e64 v143, v143, v105, s[8:9]
	v_cmp_eq_u32_e32 vcc, v113, v4
	v_cmp_eq_u32_e64 s[0:1], v121, v4
	v_cmp_eq_u32_e64 s[6:7], v129, v4
	v_cmp_eq_u32_e64 s[8:9], v137, v4
	v_cndmask_b32_e32 v119, v119, v106, vcc
	v_cndmask_b32_e64 v127, v127, v106, s[0:1]
	v_cndmask_b32_e64 v135, v135, v106, s[6:7]
	v_cndmask_b32_e64 v143, v143, v106, s[8:9]
	v_cmp_eq_u32_e32 vcc, v113, v5
	v_cmp_eq_u32_e64 s[0:1], v121, v5
	v_cmp_eq_u32_e64 s[6:7], v129, v5
	v_cmp_eq_u32_e64 s[8:9], v137, v5
	v_cndmask_b32_e32 v119, v119, v107, vcc
	v_cndmask_b32_e64 v127, v127, v107, s[0:1]
	v_cndmask_b32_e64 v135, v135, v107, s[6:7]
	v_cndmask_b32_e64 v143, v143, v107, s[8:9]
	v_cmp_gt_i32_e32 vcc, 0, v6
	s_cbranch_vccnz .Lprep_a_m5
	v_cmp_eq_u32_e32 vcc, v113, v6
	v_cmp_eq_u32_e64 s[0:1], v121, v6
	v_cmp_eq_u32_e64 s[6:7], v129, v6
	v_cmp_eq_u32_e64 s[8:9], v137, v6
	v_cndmask_b32_e32 v119, v119, v108, vcc
	v_cndmask_b32_e64 v127, v127, v108, s[0:1]
	v_cndmask_b32_e64 v135, v135, v108, s[6:7]
	v_cndmask_b32_e64 v143, v143, v108, s[8:9]
	v_cmp_eq_u32_e32 vcc, v113, v7
	v_cmp_eq_u32_e64 s[0:1], v121, v7
	v_cmp_eq_u32_e64 s[6:7], v129, v7
	v_cmp_eq_u32_e64 s[8:9], v137, v7
	v_cndmask_b32_e32 v119, v119, v109, vcc
	v_cndmask_b32_e64 v127, v127, v109, s[0:1]
	v_cndmask_b32_e64 v135, v135, v109, s[6:7]
	v_cndmask_b32_e64 v143, v143, v109, s[8:9]
	v_cmp_eq_u32_e32 vcc, v113, v8
	v_cmp_eq_u32_e64 s[0:1], v121, v8
	v_cmp_eq_u32_e64 s[6:7], v129, v8
	v_cmp_eq_u32_e64 s[8:9], v137, v8
	v_cndmask_b32_e32 v119, v119, v110, vcc
	v_cndmask_b32_e64 v127, v127, v110, s[0:1]
	v_cndmask_b32_e64 v135, v135, v110, s[6:7]
	v_cndmask_b32_e64 v143, v143, v110, s[8:9]
	v_cmp_eq_u32_e32 vcc, v113, v9
	v_cmp_eq_u32_e64 s[0:1], v121, v9
	v_cmp_eq_u32_e64 s[6:7], v129, v9
	v_cmp_eq_u32_e64 s[8:9], v137, v9
	v_cndmask_b32_e32 v119, v119, v111, vcc
	v_cndmask_b32_e64 v127, v127, v111, s[0:1]
	v_cndmask_b32_e64 v135, v135, v111, s[6:7]
	v_cndmask_b32_e64 v143, v143, v111, s[8:9]
.Lprep_a_m5:
	v_add_u32_e32 v112, v112, v119
	v_add_u32_e32 v120, v120, v127
	v_add_u32_e32 v128, v128, v135
	v_add_u32_e32 v136, v136, v143
	v_cmp_ne_u32_e32 vcc, -1, v119
	s_and_saveexec_b64 s[24:25], vcc
	ds_write_b32 v112, v114
	s_mov_b64 exec, s[24:25]
	v_cmp_ne_u32_e32 vcc, -1, v127
	s_and_saveexec_b64 s[24:25], vcc
	ds_write_b32 v120, v122
	s_mov_b64 exec, s[24:25]
	v_cmp_ne_u32_e32 vcc, -1, v135
	s_and_saveexec_b64 s[24:25], vcc
	ds_write_b32 v128, v130
	s_mov_b64 exec, s[24:25]
	v_cmp_ne_u32_e32 vcc, -1, v143
	s_and_saveexec_b64 s[24:25], vcc
	ds_write_b32 v136, v138
	s_mov_b64 exec, s[24:25]
	v_and_b32_e32 v112, 0xff, v64
	v_and_b32_e32 v120, 0xff, v65
	v_and_b32_e32 v128, 0xff, v66
	v_and_b32_e32 v136, 0xff, v67
	v_lshlrev_b32_e32 v112, 2, v112
	v_lshlrev_b32_e32 v120, 2, v120
	v_lshlrev_b32_e32 v128, 2, v128
	v_lshlrev_b32_e32 v136, 2, v136
	v_add_u32_e32 v118, v112, v11
	v_add_u32_e32 v126, v120, v11
	v_add_u32_e32 v134, v128, v11
	v_add_u32_e32 v142, v136, v11
	ds_read_b32 v113, v112 offset:36864
	ds_read_b32 v114, v112 offset:35584
	ds_read_b32 v115, v118 offset:12288
	ds_read_b32 v121, v120 offset:36864
	ds_read_b32 v122, v120 offset:35584
	ds_read_b32 v123, v126 offset:12800
	ds_read_b32 v129, v128 offset:36864
	ds_read_b32 v130, v128 offset:35584
	ds_read_b32 v131, v134 offset:13312
	ds_read_b32 v137, v136 offset:36864
	ds_read_b32 v138, v136 offset:35584
	ds_read_b32 v139, v142 offset:13824
	v_mov_b32_e32 v117, v37
	v_add_u32_e32 v37, 4, v37
	v_subrev_u32_e32 v118, s11, v37
	v_min_u32_e32 v37, v37, v118
	v_subrev_u32_e32 v118, s11, v37
	v_min_u32_e32 v37, v37, v118
	v_mov_b32_e32 v125, v37
	v_add_u32_e32 v37, 4, v37
	v_subrev_u32_e32 v126, s11, v37
	v_min_u32_e32 v37, v37, v126
	v_subrev_u32_e32 v126, s11, v37
	v_min_u32_e32 v37, v37, v126
	v_mov_b32_e32 v133, v37
	v_add_u32_e32 v37, 4, v37
	v_subrev_u32_e32 v134, s11, v37
	v_min_u32_e32 v37, v37, v134
	v_subrev_u32_e32 v134, s11, v37
	v_min_u32_e32 v37, v37, v134
	v_mov_b32_e32 v141, v37
	v_add_u32_e32 v37, 4, v37
	v_subrev_u32_e32 v142, s11, v37
	v_min_u32_e32 v37, v37, v142
	v_subrev_u32_e32 v142, s11, v37
	v_min_u32_e32 v37, v37, v142
	v_ashrrev_i32_e32 v116, 8, v64
	v_ashrrev_i32_e32 v124, 8, v65
	v_ashrrev_i32_e32 v132, 8, v66
	v_ashrrev_i32_e32 v140, 8, v67
	s_waitcnt lgkmcnt(0)
	v_add_u32_e32 v116, v116, v113
	v_add_u32_e32 v124, v124, v121
	v_add_u32_e32 v132, v132, v129
	v_add_u32_e32 v140, v140, v137
	v_add3_u32 v116, v116, v114, v115
	v_add3_u32 v124, v124, v122, v123
	v_add3_u32 v132, v132, v130, v131
	v_add3_u32 v140, v140, v138, v139
	v_cmp_eq_u32_e32 vcc, s93, v117
	v_add_u32_e32 v1, 0xc000, v10
	s_and_saveexec_b64 s[24:25], vcc
	global_store_dword v1, v116, s[16:17]
	s_mov_b64 exec, s[24:25]
	v_cmp_eq_u32_e32 vcc, s93, v125
	v_add_u32_e32 v1, 0xc800, v10
	s_and_saveexec_b64 s[24:25], vcc
	global_store_dword v1, v124, s[16:17]
	s_mov_b64 exec, s[24:25]
	v_cmp_eq_u32_e32 vcc, s93, v133
	v_add_u32_e32 v1, 0xd000, v10
	s_and_saveexec_b64 s[24:25], vcc
	global_store_dword v1, v132, s[16:17]
	s_mov_b64 exec, s[24:25]
	v_cmp_eq_u32_e32 vcc, s93, v141
	v_add_u32_e32 v1, 0xd800, v10
	s_and_saveexec_b64 s[24:25], vcc
	global_store_dword v1, v140, s[16:17]
	s_mov_b64 exec, s[24:25]
	v_ashrrev_i32_e32 v113, 8, v116
	v_ashrrev_i32_e32 v121, 8, v124
	v_ashrrev_i32_e32 v129, 8, v132
	v_ashrrev_i32_e32 v137, 8, v140
	v_and_b32_e32 v112, 0xff, v116
	v_and_b32_e32 v120, 0xff, v124
	v_and_b32_e32 v128, 0xff, v132
	v_and_b32_e32 v136, 0xff, v140
	v_lshl_add_u32 v112, v112, 2, s10
	v_lshl_add_u32 v120, v120, 2, s10
	v_lshl_add_u32 v128, v128, 2, s10
	v_lshl_add_u32 v136, v136, 2, s10
	v_add_u32_e32 v114, 0x1800, v34
	v_add_u32_e32 v122, 0x1900, v34
	v_add_u32_e32 v130, 0x1a00, v34
	v_add_u32_e32 v138, 0x1b00, v34
	v_mov_b32_e32 v119, -1
	v_mov_b32_e32 v127, -1
	v_mov_b32_e32 v135, -1
	v_mov_b32_e32 v143, -1
	v_cmp_eq_u32_e32 vcc, v113, v2
	v_cmp_eq_u32_e64 s[0:1], v121, v2
	v_cmp_eq_u32_e64 s[6:7], v129, v2
	v_cmp_eq_u32_e64 s[8:9], v137, v2
	v_cndmask_b32_e32 v119, v119, v104, vcc
	v_cndmask_b32_e64 v127, v127, v104, s[0:1]
	v_cndmask_b32_e64 v135, v135, v104, s[6:7]
	v_cndmask_b32_e64 v143, v143, v104, s[8:9]
	v_cmp_eq_u32_e32 vcc, v113, v3
	v_cmp_eq_u32_e64 s[0:1], v121, v3
	v_cmp_eq_u32_e64 s[6:7], v129, v3
	v_cmp_eq_u32_e64 s[8:9], v137, v3
	v_cndmask_b32_e32 v119, v119, v105, vcc
	v_cndmask_b32_e64 v127, v127, v105, s[0:1]
	v_cndmask_b32_e64 v135, v135, v105, s[6:7]
	v_cndmask_b32_e64 v143, v143, v105, s[8:9]
	v_cmp_eq_u32_e32 vcc, v113, v4
	v_cmp_eq_u32_e64 s[0:1], v121, v4
	v_cmp_eq_u32_e64 s[6:7], v129, v4
	v_cmp_eq_u32_e64 s[8:9], v137, v4
	v_cndmask_b32_e32 v119, v119, v106, vcc
	v_cndmask_b32_e64 v127, v127, v106, s[0:1]
	v_cndmask_b32_e64 v135, v135, v106, s[6:7]
	v_cndmask_b32_e64 v143, v143, v106, s[8:9]
	v_cmp_eq_u32_e32 vcc, v113, v5
	v_cmp_eq_u32_e64 s[0:1], v121, v5
	v_cmp_eq_u32_e64 s[6:7], v129, v5
	v_cmp_eq_u32_e64 s[8:9], v137, v5
	v_cndmask_b32_e32 v119, v119, v107, vcc
	v_cndmask_b32_e64 v127, v127, v107, s[0:1]
	v_cndmask_b32_e64 v135, v135, v107, s[6:7]
	v_cndmask_b32_e64 v143, v143, v107, s[8:9]
	v_cmp_gt_i32_e32 vcc, 0, v6
	s_cbranch_vccnz .Lprep_a_m6
	v_cmp_eq_u32_e32 vcc, v113, v6
	v_cmp_eq_u32_e64 s[0:1], v121, v6
	v_cmp_eq_u32_e64 s[6:7], v129, v6
	v_cmp_eq_u32_e64 s[8:9], v137, v6
	v_cndmask_b32_e32 v119, v119, v108, vcc
	v_cndmask_b32_e64 v127, v127, v108, s[0:1]
	v_cndmask_b32_e64 v135, v135, v108, s[6:7]
	v_cndmask_b32_e64 v143, v143, v108, s[8:9]
	v_cmp_eq_u32_e32 vcc, v113, v7
	v_cmp_eq_u32_e64 s[0:1], v121, v7
	v_cmp_eq_u32_e64 s[6:7], v129, v7
	v_cmp_eq_u32_e64 s[8:9], v137, v7
	v_cndmask_b32_e32 v119, v119, v109, vcc
	v_cndmask_b32_e64 v127, v127, v109, s[0:1]
	v_cndmask_b32_e64 v135, v135, v109, s[6:7]
	v_cndmask_b32_e64 v143, v143, v109, s[8:9]
	v_cmp_eq_u32_e32 vcc, v113, v8
	v_cmp_eq_u32_e64 s[0:1], v121, v8
	v_cmp_eq_u32_e64 s[6:7], v129, v8
	v_cmp_eq_u32_e64 s[8:9], v137, v8
	v_cndmask_b32_e32 v119, v119, v110, vcc
	v_cndmask_b32_e64 v127, v127, v110, s[0:1]
	v_cndmask_b32_e64 v135, v135, v110, s[6:7]
	v_cndmask_b32_e64 v143, v143, v110, s[8:9]
	v_cmp_eq_u32_e32 vcc, v113, v9
	v_cmp_eq_u32_e64 s[0:1], v121, v9
	v_cmp_eq_u32_e64 s[6:7], v129, v9
	v_cmp_eq_u32_e64 s[8:9], v137, v9
	v_cndmask_b32_e32 v119, v119, v111, vcc
	v_cndmask_b32_e64 v127, v127, v111, s[0:1]
	v_cndmask_b32_e64 v135, v135, v111, s[6:7]
	v_cndmask_b32_e64 v143, v143, v111, s[8:9]
.Lprep_a_m6:
	v_add_u32_e32 v112, v112, v119
	v_add_u32_e32 v120, v120, v127
	v_add_u32_e32 v128, v128, v135
	v_add_u32_e32 v136, v136, v143
	v_cmp_ne_u32_e32 vcc, -1, v119
	s_and_saveexec_b64 s[24:25], vcc
	ds_write_b32 v112, v114
	s_mov_b64 exec, s[24:25]
	v_cmp_ne_u32_e32 vcc, -1, v127
	s_and_saveexec_b64 s[24:25], vcc
	ds_write_b32 v120, v122
	s_mov_b64 exec, s[24:25]
	v_cmp_ne_u32_e32 vcc, -1, v135
	s_and_saveexec_b64 s[24:25], vcc
	ds_write_b32 v128, v130
	s_mov_b64 exec, s[24:25]
	v_cmp_ne_u32_e32 vcc, -1, v143
	s_and_saveexec_b64 s[24:25], vcc
	ds_write_b32 v136, v138
	s_mov_b64 exec, s[24:25]
	v_and_b32_e32 v112, 0xff, v68
	v_and_b32_e32 v120, 0xff, v69
	v_and_b32_e32 v128, 0xff, v70
	v_and_b32_e32 v136, 0xff, v71
	v_lshlrev_b32_e32 v112, 2, v112
	v_lshlrev_b32_e32 v120, 2, v120
	v_lshlrev_b32_e32 v128, 2, v128
	v_lshlrev_b32_e32 v136, 2, v136
	v_add_u32_e32 v118, v112, v11
	v_add_u32_e32 v126, v120, v11
	v_add_u32_e32 v134, v128, v11
	v_add_u32_e32 v142, v136, v11
	ds_read_b32 v113, v112 offset:36864
	ds_read_b32 v114, v112 offset:35712
	ds_read_b32 v115, v118 offset:14336
	ds_read_b32 v121, v120 offset:36864
	ds_read_b32 v122, v120 offset:35712
	ds_read_b32 v123, v126 offset:14848
	ds_read_b32 v129, v128 offset:36864
	ds_read_b32 v130, v128 offset:35712
	ds_read_b32 v131, v134 offset:15360
	ds_read_b32 v137, v136 offset:36864
	ds_read_b32 v138, v136 offset:35712
	ds_read_b32 v139, v142 offset:15872
	v_mov_b32_e32 v117, v37
	v_add_u32_e32 v37, 4, v37
	v_subrev_u32_e32 v118, s11, v37
	v_min_u32_e32 v37, v37, v118
	v_subrev_u32_e32 v118, s11, v37
	v_min_u32_e32 v37, v37, v118
	v_mov_b32_e32 v125, v37
	v_add_u32_e32 v37, 4, v37
	v_subrev_u32_e32 v126, s11, v37
	v_min_u32_e32 v37, v37, v126
	v_subrev_u32_e32 v126, s11, v37
	v_min_u32_e32 v37, v37, v126
	v_mov_b32_e32 v133, v37
	v_add_u32_e32 v37, 4, v37
	v_subrev_u32_e32 v134, s11, v37
	v_min_u32_e32 v37, v37, v134
	v_subrev_u32_e32 v134, s11, v37
	v_min_u32_e32 v37, v37, v134
	v_mov_b32_e32 v141, v37
	v_add_u32_e32 v37, 4, v37
	v_subrev_u32_e32 v142, s11, v37
	v_min_u32_e32 v37, v37, v142
	v_subrev_u32_e32 v142, s11, v37
	v_min_u32_e32 v37, v37, v142
	v_ashrrev_i32_e32 v116, 8, v68
	v_ashrrev_i32_e32 v124, 8, v69
	v_ashrrev_i32_e32 v132, 8, v70
	v_ashrrev_i32_e32 v140, 8, v71
	s_waitcnt lgkmcnt(0)
	v_add_u32_e32 v116, v116, v113
	v_add_u32_e32 v124, v124, v121
	v_add_u32_e32 v132, v132, v129
	v_add_u32_e32 v140, v140, v137
	v_add3_u32 v116, v116, v114, v115
	v_add3_u32 v124, v124, v122, v123
	v_add3_u32 v132, v132, v130, v131
	v_add3_u32 v140, v140, v138, v139
	v_cmp_eq_u32_e32 vcc, s93, v117
	v_add_u32_e32 v1, 0xe000, v10
	s_and_saveexec_b64 s[24:25], vcc
	global_store_dword v1, v116, s[16:17]
	s_mov_b64 exec, s[24:25]
	v_cmp_eq_u32_e32 vcc, s93, v125
	v_add_u32_e32 v1, 0xe800, v10
	s_and_saveexec_b64 s[24:25], vcc
	global_store_dword v1, v124, s[16:17]
	s_mov_b64 exec, s[24:25]
	v_cmp_eq_u32_e32 vcc, s93, v133
	v_add_u32_e32 v1, 0xf000, v10
	s_and_saveexec_b64 s[24:25], vcc
	global_store_dword v1, v132, s[16:17]
	s_mov_b64 exec, s[24:25]
	v_cmp_eq_u32_e32 vcc, s93, v141
	v_add_u32_e32 v1, 0xf800, v10
	s_and_saveexec_b64 s[24:25], vcc
	global_store_dword v1, v140, s[16:17]
	s_mov_b64 exec, s[24:25]
	v_ashrrev_i32_e32 v113, 8, v116
	v_ashrrev_i32_e32 v121, 8, v124
	v_ashrrev_i32_e32 v129, 8, v132
	v_ashrrev_i32_e32 v137, 8, v140
	v_and_b32_e32 v112, 0xff, v116
	v_and_b32_e32 v120, 0xff, v124
	v_and_b32_e32 v128, 0xff, v132
	v_and_b32_e32 v136, 0xff, v140
	v_lshl_add_u32 v112, v112, 2, s10
	v_lshl_add_u32 v120, v120, 2, s10
	v_lshl_add_u32 v128, v128, 2, s10
	v_lshl_add_u32 v136, v136, 2, s10
	v_add_u32_e32 v114, 0x1c00, v34
	v_add_u32_e32 v122, 0x1d00, v34
	v_add_u32_e32 v130, 0x1e00, v34
	v_add_u32_e32 v138, 0x1f00, v34
	v_mov_b32_e32 v119, -1
	v_mov_b32_e32 v127, -1
	v_mov_b32_e32 v135, -1
	v_mov_b32_e32 v143, -1
	v_cmp_eq_u32_e32 vcc, v113, v2
	v_cmp_eq_u32_e64 s[0:1], v121, v2
	v_cmp_eq_u32_e64 s[6:7], v129, v2
	v_cmp_eq_u32_e64 s[8:9], v137, v2
	v_cndmask_b32_e32 v119, v119, v104, vcc
	v_cndmask_b32_e64 v127, v127, v104, s[0:1]
	v_cndmask_b32_e64 v135, v135, v104, s[6:7]
	v_cndmask_b32_e64 v143, v143, v104, s[8:9]
	v_cmp_eq_u32_e32 vcc, v113, v3
	v_cmp_eq_u32_e64 s[0:1], v121, v3
	v_cmp_eq_u32_e64 s[6:7], v129, v3
	v_cmp_eq_u32_e64 s[8:9], v137, v3
	v_cndmask_b32_e32 v119, v119, v105, vcc
	v_cndmask_b32_e64 v127, v127, v105, s[0:1]
	v_cndmask_b32_e64 v135, v135, v105, s[6:7]
	v_cndmask_b32_e64 v143, v143, v105, s[8:9]
	v_cmp_eq_u32_e32 vcc, v113, v4
	v_cmp_eq_u32_e64 s[0:1], v121, v4
	v_cmp_eq_u32_e64 s[6:7], v129, v4
	v_cmp_eq_u32_e64 s[8:9], v137, v4
	v_cndmask_b32_e32 v119, v119, v106, vcc
	v_cndmask_b32_e64 v127, v127, v106, s[0:1]
	v_cndmask_b32_e64 v135, v135, v106, s[6:7]
	v_cndmask_b32_e64 v143, v143, v106, s[8:9]
	v_cmp_eq_u32_e32 vcc, v113, v5
	v_cmp_eq_u32_e64 s[0:1], v121, v5
	v_cmp_eq_u32_e64 s[6:7], v129, v5
	v_cmp_eq_u32_e64 s[8:9], v137, v5
	v_cndmask_b32_e32 v119, v119, v107, vcc
	v_cndmask_b32_e64 v127, v127, v107, s[0:1]
	v_cndmask_b32_e64 v135, v135, v107, s[6:7]
	v_cndmask_b32_e64 v143, v143, v107, s[8:9]
	v_cmp_gt_i32_e32 vcc, 0, v6
	s_cbranch_vccnz .Lprep_a_m7
	v_cmp_eq_u32_e32 vcc, v113, v6
	v_cmp_eq_u32_e64 s[0:1], v121, v6
	v_cmp_eq_u32_e64 s[6:7], v129, v6
	v_cmp_eq_u32_e64 s[8:9], v137, v6
	v_cndmask_b32_e32 v119, v119, v108, vcc
	v_cndmask_b32_e64 v127, v127, v108, s[0:1]
	v_cndmask_b32_e64 v135, v135, v108, s[6:7]
	v_cndmask_b32_e64 v143, v143, v108, s[8:9]
	v_cmp_eq_u32_e32 vcc, v113, v7
	v_cmp_eq_u32_e64 s[0:1], v121, v7
	v_cmp_eq_u32_e64 s[6:7], v129, v7
	v_cmp_eq_u32_e64 s[8:9], v137, v7
	v_cndmask_b32_e32 v119, v119, v109, vcc
	v_cndmask_b32_e64 v127, v127, v109, s[0:1]
	v_cndmask_b32_e64 v135, v135, v109, s[6:7]
	v_cndmask_b32_e64 v143, v143, v109, s[8:9]
	v_cmp_eq_u32_e32 vcc, v113, v8
	v_cmp_eq_u32_e64 s[0:1], v121, v8
	v_cmp_eq_u32_e64 s[6:7], v129, v8
	v_cmp_eq_u32_e64 s[8:9], v137, v8
	v_cndmask_b32_e32 v119, v119, v110, vcc
	v_cndmask_b32_e64 v127, v127, v110, s[0:1]
	v_cndmask_b32_e64 v135, v135, v110, s[6:7]
	v_cndmask_b32_e64 v143, v143, v110, s[8:9]
	v_cmp_eq_u32_e32 vcc, v113, v9
	v_cmp_eq_u32_e64 s[0:1], v121, v9
	v_cmp_eq_u32_e64 s[6:7], v129, v9
	v_cmp_eq_u32_e64 s[8:9], v137, v9
	v_cndmask_b32_e32 v119, v119, v111, vcc
	v_cndmask_b32_e64 v127, v127, v111, s[0:1]
	v_cndmask_b32_e64 v135, v135, v111, s[6:7]
	v_cndmask_b32_e64 v143, v143, v111, s[8:9]
.Lprep_a_m7:
	v_add_u32_e32 v112, v112, v119
	v_add_u32_e32 v120, v120, v127
	v_add_u32_e32 v128, v128, v135
	v_add_u32_e32 v136, v136, v143
	v_cmp_ne_u32_e32 vcc, -1, v119
	s_and_saveexec_b64 s[24:25], vcc
	ds_write_b32 v112, v114
	s_mov_b64 exec, s[24:25]
	v_cmp_ne_u32_e32 vcc, -1, v127
	s_and_saveexec_b64 s[24:25], vcc
	ds_write_b32 v120, v122
	s_mov_b64 exec, s[24:25]
	v_cmp_ne_u32_e32 vcc, -1, v135
	s_and_saveexec_b64 s[24:25], vcc
	ds_write_b32 v128, v130
	s_mov_b64 exec, s[24:25]
	v_cmp_ne_u32_e32 vcc, -1, v143
	s_and_saveexec_b64 s[24:25], vcc
	ds_write_b32 v136, v138
	s_mov_b64 exec, s[24:25]
	v_and_b32_e32 v112, 0xff, v72
	v_and_b32_e32 v120, 0xff, v73
	v_and_b32_e32 v128, 0xff, v74
	v_and_b32_e32 v136, 0xff, v75
	v_lshlrev_b32_e32 v112, 2, v112
	v_lshlrev_b32_e32 v120, 2, v120
	v_lshlrev_b32_e32 v128, 2, v128
	v_lshlrev_b32_e32 v136, 2, v136
	v_add_u32_e32 v118, v112, v11
	v_add_u32_e32 v126, v120, v11
	v_add_u32_e32 v134, v128, v11
	v_add_u32_e32 v142, v136, v11
	ds_read_b32 v113, v112 offset:36864
	ds_read_b32 v114, v112 offset:35840
	ds_read_b32 v115, v118 offset:16384
	ds_read_b32 v121, v120 offset:36864
	ds_read_b32 v122, v120 offset:35840
	ds_read_b32 v123, v126 offset:16896
	ds_read_b32 v129, v128 offset:36864
	ds_read_b32 v130, v128 offset:35840
	ds_read_b32 v131, v134 offset:17408
	ds_read_b32 v137, v136 offset:36864
	ds_read_b32 v138, v136 offset:35840
	ds_read_b32 v139, v142 offset:17920
	v_mov_b32_e32 v117, v37
	v_add_u32_e32 v37, 4, v37
	v_subrev_u32_e32 v118, s11, v37
	v_min_u32_e32 v37, v37, v118
	v_subrev_u32_e32 v118, s11, v37
	v_min_u32_e32 v37, v37, v118
	v_mov_b32_e32 v125, v37
	v_add_u32_e32 v37, 4, v37
	v_subrev_u32_e32 v126, s11, v37
	v_min_u32_e32 v37, v37, v126
	v_subrev_u32_e32 v126, s11, v37
	v_min_u32_e32 v37, v37, v126
	v_mov_b32_e32 v133, v37
	v_add_u32_e32 v37, 4, v37
	v_subrev_u32_e32 v134, s11, v37
	v_min_u32_e32 v37, v37, v134
	v_subrev_u32_e32 v134, s11, v37
	v_min_u32_e32 v37, v37, v134
	v_mov_b32_e32 v141, v37
	v_add_u32_e32 v37, 4, v37
	v_subrev_u32_e32 v142, s11, v37
	v_min_u32_e32 v37, v37, v142
	v_subrev_u32_e32 v142, s11, v37
	v_min_u32_e32 v37, v37, v142
	v_ashrrev_i32_e32 v116, 8, v72
	v_ashrrev_i32_e32 v124, 8, v73
	v_ashrrev_i32_e32 v132, 8, v74
	v_ashrrev_i32_e32 v140, 8, v75
	s_waitcnt lgkmcnt(0)
	v_add_u32_e32 v116, v116, v113
	v_add_u32_e32 v124, v124, v121
	v_add_u32_e32 v132, v132, v129
	v_add_u32_e32 v140, v140, v137
	v_add3_u32 v116, v116, v114, v115
	v_add3_u32 v124, v124, v122, v123
	v_add3_u32 v132, v132, v130, v131
	v_add3_u32 v140, v140, v138, v139
	v_cmp_eq_u32_e32 vcc, s93, v117
	v_add_u32_e32 v1, 0x10000, v10
	s_and_saveexec_b64 s[24:25], vcc
	global_store_dword v1, v116, s[16:17]
	s_mov_b64 exec, s[24:25]
	v_cmp_eq_u32_e32 vcc, s93, v125
	v_add_u32_e32 v1, 0x10800, v10
	s_and_saveexec_b64 s[24:25], vcc
	global_store_dword v1, v124, s[16:17]
	s_mov_b64 exec, s[24:25]
	v_cmp_eq_u32_e32 vcc, s93, v133
	v_add_u32_e32 v1, 0x11000, v10
	s_and_saveexec_b64 s[24:25], vcc
	global_store_dword v1, v132, s[16:17]
	s_mov_b64 exec, s[24:25]
	v_cmp_eq_u32_e32 vcc, s93, v141
	v_add_u32_e32 v1, 0x11800, v10
	s_and_saveexec_b64 s[24:25], vcc
	global_store_dword v1, v140, s[16:17]
	s_mov_b64 exec, s[24:25]
	v_ashrrev_i32_e32 v113, 8, v116
	v_ashrrev_i32_e32 v121, 8, v124
	v_ashrrev_i32_e32 v129, 8, v132
	v_ashrrev_i32_e32 v137, 8, v140
	v_and_b32_e32 v112, 0xff, v116
	v_and_b32_e32 v120, 0xff, v124
	v_and_b32_e32 v128, 0xff, v132
	v_and_b32_e32 v136, 0xff, v140
	v_lshl_add_u32 v112, v112, 2, s10
	v_lshl_add_u32 v120, v120, 2, s10
	v_lshl_add_u32 v128, v128, 2, s10
	v_lshl_add_u32 v136, v136, 2, s10
	v_add_u32_e32 v114, 0x2000, v34
	v_add_u32_e32 v122, 0x2100, v34
	v_add_u32_e32 v130, 0x2200, v34
	v_add_u32_e32 v138, 0x2300, v34
	v_mov_b32_e32 v119, -1
	v_mov_b32_e32 v127, -1
	v_mov_b32_e32 v135, -1
	v_mov_b32_e32 v143, -1
	v_cmp_eq_u32_e32 vcc, v113, v2
	v_cmp_eq_u32_e64 s[0:1], v121, v2
	v_cmp_eq_u32_e64 s[6:7], v129, v2
	v_cmp_eq_u32_e64 s[8:9], v137, v2
	v_cndmask_b32_e32 v119, v119, v104, vcc
	v_cndmask_b32_e64 v127, v127, v104, s[0:1]
	v_cndmask_b32_e64 v135, v135, v104, s[6:7]
	v_cndmask_b32_e64 v143, v143, v104, s[8:9]
	v_cmp_eq_u32_e32 vcc, v113, v3
	v_cmp_eq_u32_e64 s[0:1], v121, v3
	v_cmp_eq_u32_e64 s[6:7], v129, v3
	v_cmp_eq_u32_e64 s[8:9], v137, v3
	v_cndmask_b32_e32 v119, v119, v105, vcc
	v_cndmask_b32_e64 v127, v127, v105, s[0:1]
	v_cndmask_b32_e64 v135, v135, v105, s[6:7]
	v_cndmask_b32_e64 v143, v143, v105, s[8:9]
	v_cmp_eq_u32_e32 vcc, v113, v4
	v_cmp_eq_u32_e64 s[0:1], v121, v4
	v_cmp_eq_u32_e64 s[6:7], v129, v4
	v_cmp_eq_u32_e64 s[8:9], v137, v4
	v_cndmask_b32_e32 v119, v119, v106, vcc
	v_cndmask_b32_e64 v127, v127, v106, s[0:1]
	v_cndmask_b32_e64 v135, v135, v106, s[6:7]
	v_cndmask_b32_e64 v143, v143, v106, s[8:9]
	v_cmp_eq_u32_e32 vcc, v113, v5
	v_cmp_eq_u32_e64 s[0:1], v121, v5
	v_cmp_eq_u32_e64 s[6:7], v129, v5
	v_cmp_eq_u32_e64 s[8:9], v137, v5
	v_cndmask_b32_e32 v119, v119, v107, vcc
	v_cndmask_b32_e64 v127, v127, v107, s[0:1]
	v_cndmask_b32_e64 v135, v135, v107, s[6:7]
	v_cndmask_b32_e64 v143, v143, v107, s[8:9]
	v_cmp_gt_i32_e32 vcc, 0, v6
	s_cbranch_vccnz .Lprep_a_m8
	v_cmp_eq_u32_e32 vcc, v113, v6
	v_cmp_eq_u32_e64 s[0:1], v121, v6
	v_cmp_eq_u32_e64 s[6:7], v129, v6
	v_cmp_eq_u32_e64 s[8:9], v137, v6
	v_cndmask_b32_e32 v119, v119, v108, vcc
	v_cndmask_b32_e64 v127, v127, v108, s[0:1]
	v_cndmask_b32_e64 v135, v135, v108, s[6:7]
	v_cndmask_b32_e64 v143, v143, v108, s[8:9]
	v_cmp_eq_u32_e32 vcc, v113, v7
	v_cmp_eq_u32_e64 s[0:1], v121, v7
	v_cmp_eq_u32_e64 s[6:7], v129, v7
	v_cmp_eq_u32_e64 s[8:9], v137, v7
	v_cndmask_b32_e32 v119, v119, v109, vcc
	v_cndmask_b32_e64 v127, v127, v109, s[0:1]
	v_cndmask_b32_e64 v135, v135, v109, s[6:7]
	v_cndmask_b32_e64 v143, v143, v109, s[8:9]
	v_cmp_eq_u32_e32 vcc, v113, v8
	v_cmp_eq_u32_e64 s[0:1], v121, v8
	v_cmp_eq_u32_e64 s[6:7], v129, v8
	v_cmp_eq_u32_e64 s[8:9], v137, v8
	v_cndmask_b32_e32 v119, v119, v110, vcc
	v_cndmask_b32_e64 v127, v127, v110, s[0:1]
	v_cndmask_b32_e64 v135, v135, v110, s[6:7]
	v_cndmask_b32_e64 v143, v143, v110, s[8:9]
	v_cmp_eq_u32_e32 vcc, v113, v9
	v_cmp_eq_u32_e64 s[0:1], v121, v9
	v_cmp_eq_u32_e64 s[6:7], v129, v9
	v_cmp_eq_u32_e64 s[8:9], v137, v9
	v_cndmask_b32_e32 v119, v119, v111, vcc
	v_cndmask_b32_e64 v127, v127, v111, s[0:1]
	v_cndmask_b32_e64 v135, v135, v111, s[6:7]
	v_cndmask_b32_e64 v143, v143, v111, s[8:9]
.Lprep_a_m8:
	v_add_u32_e32 v112, v112, v119
	v_add_u32_e32 v120, v120, v127
	v_add_u32_e32 v128, v128, v135
	v_add_u32_e32 v136, v136, v143
	v_cmp_ne_u32_e32 vcc, -1, v119
	s_and_saveexec_b64 s[24:25], vcc
	ds_write_b32 v112, v114
	s_mov_b64 exec, s[24:25]
	v_cmp_ne_u32_e32 vcc, -1, v127
	s_and_saveexec_b64 s[24:25], vcc
	ds_write_b32 v120, v122
	s_mov_b64 exec, s[24:25]
	v_cmp_ne_u32_e32 vcc, -1, v135
	s_and_saveexec_b64 s[24:25], vcc
	ds_write_b32 v128, v130
	s_mov_b64 exec, s[24:25]
	v_cmp_ne_u32_e32 vcc, -1, v143
	s_and_saveexec_b64 s[24:25], vcc
	ds_write_b32 v136, v138
	s_mov_b64 exec, s[24:25]
	v_and_b32_e32 v112, 0xff, v76
	v_and_b32_e32 v120, 0xff, v77
	v_and_b32_e32 v128, 0xff, v78
	v_and_b32_e32 v136, 0xff, v79
	v_lshlrev_b32_e32 v112, 2, v112
	v_lshlrev_b32_e32 v120, 2, v120
	v_lshlrev_b32_e32 v128, 2, v128
	v_lshlrev_b32_e32 v136, 2, v136
	v_add_u32_e32 v118, v112, v11
	v_add_u32_e32 v126, v120, v11
	v_add_u32_e32 v134, v128, v11
	v_add_u32_e32 v142, v136, v11
	ds_read_b32 v113, v112 offset:36864
	ds_read_b32 v114, v112 offset:35968
	ds_read_b32 v115, v118 offset:18432
	ds_read_b32 v121, v120 offset:36864
	ds_read_b32 v122, v120 offset:35968
	ds_read_b32 v123, v126 offset:18944
	ds_read_b32 v129, v128 offset:36864
	ds_read_b32 v130, v128 offset:35968
	ds_read_b32 v131, v134 offset:19456
	ds_read_b32 v137, v136 offset:36864
	ds_read_b32 v138, v136 offset:35968
	ds_read_b32 v139, v142 offset:19968
	v_mov_b32_e32 v117, v37
	v_add_u32_e32 v37, 4, v37
	v_subrev_u32_e32 v118, s11, v37
	v_min_u32_e32 v37, v37, v118
	v_subrev_u32_e32 v118, s11, v37
	v_min_u32_e32 v37, v37, v118
	v_mov_b32_e32 v125, v37
	v_add_u32_e32 v37, 4, v37
	v_subrev_u32_e32 v126, s11, v37
	v_min_u32_e32 v37, v37, v126
	v_subrev_u32_e32 v126, s11, v37
	v_min_u32_e32 v37, v37, v126
	v_mov_b32_e32 v133, v37
	v_add_u32_e32 v37, 4, v37
	v_subrev_u32_e32 v134, s11, v37
	v_min_u32_e32 v37, v37, v134
	v_subrev_u32_e32 v134, s11, v37
	v_min_u32_e32 v37, v37, v134
	v_mov_b32_e32 v141, v37
	v_add_u32_e32 v37, 4, v37
	v_subrev_u32_e32 v142, s11, v37
	v_min_u32_e32 v37, v37, v142
	v_subrev_u32_e32 v142, s11, v37
	v_min_u32_e32 v37, v37, v142
	v_ashrrev_i32_e32 v116, 8, v76
	v_ashrrev_i32_e32 v124, 8, v77
	v_ashrrev_i32_e32 v132, 8, v78
	v_ashrrev_i32_e32 v140, 8, v79
	s_waitcnt lgkmcnt(0)
	v_add_u32_e32 v116, v116, v113
	v_add_u32_e32 v124, v124, v121
	v_add_u32_e32 v132, v132, v129
	v_add_u32_e32 v140, v140, v137
	v_add3_u32 v116, v116, v114, v115
	v_add3_u32 v124, v124, v122, v123
	v_add3_u32 v132, v132, v130, v131
	v_add3_u32 v140, v140, v138, v139
	v_cmp_eq_u32_e32 vcc, s93, v117
	v_add_u32_e32 v1, 0x12000, v10
	s_and_saveexec_b64 s[24:25], vcc
	global_store_dword v1, v116, s[16:17]
	s_mov_b64 exec, s[24:25]
	v_cmp_eq_u32_e32 vcc, s93, v125
	v_add_u32_e32 v1, 0x12800, v10
	s_and_saveexec_b64 s[24:25], vcc
	global_store_dword v1, v124, s[16:17]
	s_mov_b64 exec, s[24:25]
	v_cmp_eq_u32_e32 vcc, s93, v133
	v_add_u32_e32 v1, 0x13000, v10
	s_and_saveexec_b64 s[24:25], vcc
	global_store_dword v1, v132, s[16:17]
	s_mov_b64 exec, s[24:25]
	v_cmp_eq_u32_e32 vcc, s93, v141
	v_add_u32_e32 v1, 0x13800, v10
	s_and_saveexec_b64 s[24:25], vcc
	global_store_dword v1, v140, s[16:17]
	s_mov_b64 exec, s[24:25]
	v_ashrrev_i32_e32 v113, 8, v116
	v_ashrrev_i32_e32 v121, 8, v124
	v_ashrrev_i32_e32 v129, 8, v132
	v_ashrrev_i32_e32 v137, 8, v140
	v_and_b32_e32 v112, 0xff, v116
	v_and_b32_e32 v120, 0xff, v124
	v_and_b32_e32 v128, 0xff, v132
	v_and_b32_e32 v136, 0xff, v140
	v_lshl_add_u32 v112, v112, 2, s10
	v_lshl_add_u32 v120, v120, 2, s10
	v_lshl_add_u32 v128, v128, 2, s10
	v_lshl_add_u32 v136, v136, 2, s10
	v_add_u32_e32 v114, 0x2400, v34
	v_add_u32_e32 v122, 0x2500, v34
	v_add_u32_e32 v130, 0x2600, v34
	v_add_u32_e32 v138, 0x2700, v34
	v_mov_b32_e32 v119, -1
	v_mov_b32_e32 v127, -1
	v_mov_b32_e32 v135, -1
	v_mov_b32_e32 v143, -1
	v_cmp_eq_u32_e32 vcc, v113, v2
	v_cmp_eq_u32_e64 s[0:1], v121, v2
	v_cmp_eq_u32_e64 s[6:7], v129, v2
	v_cmp_eq_u32_e64 s[8:9], v137, v2
	v_cndmask_b32_e32 v119, v119, v104, vcc
	v_cndmask_b32_e64 v127, v127, v104, s[0:1]
	v_cndmask_b32_e64 v135, v135, v104, s[6:7]
	v_cndmask_b32_e64 v143, v143, v104, s[8:9]
	v_cmp_eq_u32_e32 vcc, v113, v3
	v_cmp_eq_u32_e64 s[0:1], v121, v3
	v_cmp_eq_u32_e64 s[6:7], v129, v3
	v_cmp_eq_u32_e64 s[8:9], v137, v3
	v_cndmask_b32_e32 v119, v119, v105, vcc
	v_cndmask_b32_e64 v127, v127, v105, s[0:1]
	v_cndmask_b32_e64 v135, v135, v105, s[6:7]
	v_cndmask_b32_e64 v143, v143, v105, s[8:9]
	v_cmp_eq_u32_e32 vcc, v113, v4
	v_cmp_eq_u32_e64 s[0:1], v121, v4
	v_cmp_eq_u32_e64 s[6:7], v129, v4
	v_cmp_eq_u32_e64 s[8:9], v137, v4
	v_cndmask_b32_e32 v119, v119, v106, vcc
	v_cndmask_b32_e64 v127, v127, v106, s[0:1]
	v_cndmask_b32_e64 v135, v135, v106, s[6:7]
	v_cndmask_b32_e64 v143, v143, v106, s[8:9]
	v_cmp_eq_u32_e32 vcc, v113, v5
	v_cmp_eq_u32_e64 s[0:1], v121, v5
	v_cmp_eq_u32_e64 s[6:7], v129, v5
	v_cmp_eq_u32_e64 s[8:9], v137, v5
	v_cndmask_b32_e32 v119, v119, v107, vcc
	v_cndmask_b32_e64 v127, v127, v107, s[0:1]
	v_cndmask_b32_e64 v135, v135, v107, s[6:7]
	v_cndmask_b32_e64 v143, v143, v107, s[8:9]
	v_cmp_gt_i32_e32 vcc, 0, v6
	s_cbranch_vccnz .Lprep_a_m9
	v_cmp_eq_u32_e32 vcc, v113, v6
	v_cmp_eq_u32_e64 s[0:1], v121, v6
	v_cmp_eq_u32_e64 s[6:7], v129, v6
	v_cmp_eq_u32_e64 s[8:9], v137, v6
	v_cndmask_b32_e32 v119, v119, v108, vcc
	v_cndmask_b32_e64 v127, v127, v108, s[0:1]
	v_cndmask_b32_e64 v135, v135, v108, s[6:7]
	v_cndmask_b32_e64 v143, v143, v108, s[8:9]
	v_cmp_eq_u32_e32 vcc, v113, v7
	v_cmp_eq_u32_e64 s[0:1], v121, v7
	v_cmp_eq_u32_e64 s[6:7], v129, v7
	v_cmp_eq_u32_e64 s[8:9], v137, v7
	v_cndmask_b32_e32 v119, v119, v109, vcc
	v_cndmask_b32_e64 v127, v127, v109, s[0:1]
	v_cndmask_b32_e64 v135, v135, v109, s[6:7]
	v_cndmask_b32_e64 v143, v143, v109, s[8:9]
	v_cmp_eq_u32_e32 vcc, v113, v8
	v_cmp_eq_u32_e64 s[0:1], v121, v8
	v_cmp_eq_u32_e64 s[6:7], v129, v8
	v_cmp_eq_u32_e64 s[8:9], v137, v8
	v_cndmask_b32_e32 v119, v119, v110, vcc
	v_cndmask_b32_e64 v127, v127, v110, s[0:1]
	v_cndmask_b32_e64 v135, v135, v110, s[6:7]
	v_cndmask_b32_e64 v143, v143, v110, s[8:9]
	v_cmp_eq_u32_e32 vcc, v113, v9
	v_cmp_eq_u32_e64 s[0:1], v121, v9
	v_cmp_eq_u32_e64 s[6:7], v129, v9
	v_cmp_eq_u32_e64 s[8:9], v137, v9
	v_cndmask_b32_e32 v119, v119, v111, vcc
	v_cndmask_b32_e64 v127, v127, v111, s[0:1]
	v_cndmask_b32_e64 v135, v135, v111, s[6:7]
	v_cndmask_b32_e64 v143, v143, v111, s[8:9]
.Lprep_a_m9:
	v_add_u32_e32 v112, v112, v119
	v_add_u32_e32 v120, v120, v127
	v_add_u32_e32 v128, v128, v135
	v_add_u32_e32 v136, v136, v143
	v_cmp_ne_u32_e32 vcc, -1, v119
	s_and_saveexec_b64 s[24:25], vcc
	ds_write_b32 v112, v114
	s_mov_b64 exec, s[24:25]
	v_cmp_ne_u32_e32 vcc, -1, v127
	s_and_saveexec_b64 s[24:25], vcc
	ds_write_b32 v120, v122
	s_mov_b64 exec, s[24:25]
	v_cmp_ne_u32_e32 vcc, -1, v135
	s_and_saveexec_b64 s[24:25], vcc
	ds_write_b32 v128, v130
	s_mov_b64 exec, s[24:25]
	v_cmp_ne_u32_e32 vcc, -1, v143
	s_and_saveexec_b64 s[24:25], vcc
	ds_write_b32 v136, v138
	s_mov_b64 exec, s[24:25]
	v_and_b32_e32 v112, 0xff, v80
	v_and_b32_e32 v120, 0xff, v81
	v_and_b32_e32 v128, 0xff, v82
	v_and_b32_e32 v136, 0xff, v83
	v_lshlrev_b32_e32 v112, 2, v112
	v_lshlrev_b32_e32 v120, 2, v120
	v_lshlrev_b32_e32 v128, 2, v128
	v_lshlrev_b32_e32 v136, 2, v136
	v_add_u32_e32 v118, v112, v11
	v_add_u32_e32 v126, v120, v11
	v_add_u32_e32 v134, v128, v11
	v_add_u32_e32 v142, v136, v11
	ds_read_b32 v113, v112 offset:36864
	ds_read_b32 v114, v112 offset:36096
	ds_read_b32 v115, v118 offset:20480
	ds_read_b32 v121, v120 offset:36864
	ds_read_b32 v122, v120 offset:36096
	ds_read_b32 v123, v126 offset:20992
	ds_read_b32 v129, v128 offset:36864
	ds_read_b32 v130, v128 offset:36096
	ds_read_b32 v131, v134 offset:21504
	ds_read_b32 v137, v136 offset:36864
	ds_read_b32 v138, v136 offset:36096
	ds_read_b32 v139, v142 offset:22016
	v_mov_b32_e32 v117, v37
	v_add_u32_e32 v37, 4, v37
	v_subrev_u32_e32 v118, s11, v37
	v_min_u32_e32 v37, v37, v118
	v_subrev_u32_e32 v118, s11, v37
	v_min_u32_e32 v37, v37, v118
	v_mov_b32_e32 v125, v37
	v_add_u32_e32 v37, 4, v37
	v_subrev_u32_e32 v126, s11, v37
	v_min_u32_e32 v37, v37, v126
	v_subrev_u32_e32 v126, s11, v37
	v_min_u32_e32 v37, v37, v126
	v_mov_b32_e32 v133, v37
	v_add_u32_e32 v37, 4, v37
	v_subrev_u32_e32 v134, s11, v37
	v_min_u32_e32 v37, v37, v134
	v_subrev_u32_e32 v134, s11, v37
	v_min_u32_e32 v37, v37, v134
	v_mov_b32_e32 v141, v37
	v_add_u32_e32 v37, 4, v37
	v_subrev_u32_e32 v142, s11, v37
	v_min_u32_e32 v37, v37, v142
	v_subrev_u32_e32 v142, s11, v37
	v_min_u32_e32 v37, v37, v142
	v_ashrrev_i32_e32 v116, 8, v80
	v_ashrrev_i32_e32 v124, 8, v81
	v_ashrrev_i32_e32 v132, 8, v82
	v_ashrrev_i32_e32 v140, 8, v83
	s_waitcnt lgkmcnt(0)
	v_add_u32_e32 v116, v116, v113
	v_add_u32_e32 v124, v124, v121
	v_add_u32_e32 v132, v132, v129
	v_add_u32_e32 v140, v140, v137
	v_add3_u32 v116, v116, v114, v115
	v_add3_u32 v124, v124, v122, v123
	v_add3_u32 v132, v132, v130, v131
	v_add3_u32 v140, v140, v138, v139
	v_cmp_eq_u32_e32 vcc, s93, v117
	v_add_u32_e32 v1, 0x14000, v10
	s_and_saveexec_b64 s[24:25], vcc
	global_store_dword v1, v116, s[16:17]
	s_mov_b64 exec, s[24:25]
	v_cmp_eq_u32_e32 vcc, s93, v125
	v_add_u32_e32 v1, 0x14800, v10
	s_and_saveexec_b64 s[24:25], vcc
	global_store_dword v1, v124, s[16:17]
	s_mov_b64 exec, s[24:25]
	v_cmp_eq_u32_e32 vcc, s93, v133
	v_add_u32_e32 v1, 0x15000, v10
	s_and_saveexec_b64 s[24:25], vcc
	global_store_dword v1, v132, s[16:17]
	s_mov_b64 exec, s[24:25]
	v_cmp_eq_u32_e32 vcc, s93, v141
	v_add_u32_e32 v1, 0x15800, v10
	s_and_saveexec_b64 s[24:25], vcc
	global_store_dword v1, v140, s[16:17]
	s_mov_b64 exec, s[24:25]
	v_ashrrev_i32_e32 v113, 8, v116
	v_ashrrev_i32_e32 v121, 8, v124
	v_ashrrev_i32_e32 v129, 8, v132
	v_ashrrev_i32_e32 v137, 8, v140
	v_and_b32_e32 v112, 0xff, v116
	v_and_b32_e32 v120, 0xff, v124
	v_and_b32_e32 v128, 0xff, v132
	v_and_b32_e32 v136, 0xff, v140
	v_lshl_add_u32 v112, v112, 2, s10
	v_lshl_add_u32 v120, v120, 2, s10
	v_lshl_add_u32 v128, v128, 2, s10
	v_lshl_add_u32 v136, v136, 2, s10
	v_add_u32_e32 v114, 0x2800, v34
	v_add_u32_e32 v122, 0x2900, v34
	v_add_u32_e32 v130, 0x2a00, v34
	v_add_u32_e32 v138, 0x2b00, v34
	v_mov_b32_e32 v119, -1
	v_mov_b32_e32 v127, -1
	v_mov_b32_e32 v135, -1
	v_mov_b32_e32 v143, -1
	v_cmp_eq_u32_e32 vcc, v113, v2
	v_cmp_eq_u32_e64 s[0:1], v121, v2
	v_cmp_eq_u32_e64 s[6:7], v129, v2
	v_cmp_eq_u32_e64 s[8:9], v137, v2
	v_cndmask_b32_e32 v119, v119, v104, vcc
	v_cndmask_b32_e64 v127, v127, v104, s[0:1]
	v_cndmask_b32_e64 v135, v135, v104, s[6:7]
	v_cndmask_b32_e64 v143, v143, v104, s[8:9]
	v_cmp_eq_u32_e32 vcc, v113, v3
	v_cmp_eq_u32_e64 s[0:1], v121, v3
	v_cmp_eq_u32_e64 s[6:7], v129, v3
	v_cmp_eq_u32_e64 s[8:9], v137, v3
	v_cndmask_b32_e32 v119, v119, v105, vcc
	v_cndmask_b32_e64 v127, v127, v105, s[0:1]
	v_cndmask_b32_e64 v135, v135, v105, s[6:7]
	v_cndmask_b32_e64 v143, v143, v105, s[8:9]
	v_cmp_eq_u32_e32 vcc, v113, v4
	v_cmp_eq_u32_e64 s[0:1], v121, v4
	v_cmp_eq_u32_e64 s[6:7], v129, v4
	v_cmp_eq_u32_e64 s[8:9], v137, v4
	v_cndmask_b32_e32 v119, v119, v106, vcc
	v_cndmask_b32_e64 v127, v127, v106, s[0:1]
	v_cndmask_b32_e64 v135, v135, v106, s[6:7]
	v_cndmask_b32_e64 v143, v143, v106, s[8:9]
	v_cmp_eq_u32_e32 vcc, v113, v5
	v_cmp_eq_u32_e64 s[0:1], v121, v5
	v_cmp_eq_u32_e64 s[6:7], v129, v5
	v_cmp_eq_u32_e64 s[8:9], v137, v5
	v_cndmask_b32_e32 v119, v119, v107, vcc
	v_cndmask_b32_e64 v127, v127, v107, s[0:1]
	v_cndmask_b32_e64 v135, v135, v107, s[6:7]
	v_cndmask_b32_e64 v143, v143, v107, s[8:9]
	v_cmp_gt_i32_e32 vcc, 0, v6
	s_cbranch_vccnz .Lprep_a_m10
	v_cmp_eq_u32_e32 vcc, v113, v6
	v_cmp_eq_u32_e64 s[0:1], v121, v6
	v_cmp_eq_u32_e64 s[6:7], v129, v6
	v_cmp_eq_u32_e64 s[8:9], v137, v6
	v_cndmask_b32_e32 v119, v119, v108, vcc
	v_cndmask_b32_e64 v127, v127, v108, s[0:1]
	v_cndmask_b32_e64 v135, v135, v108, s[6:7]
	v_cndmask_b32_e64 v143, v143, v108, s[8:9]
	v_cmp_eq_u32_e32 vcc, v113, v7
	v_cmp_eq_u32_e64 s[0:1], v121, v7
	v_cmp_eq_u32_e64 s[6:7], v129, v7
	v_cmp_eq_u32_e64 s[8:9], v137, v7
	v_cndmask_b32_e32 v119, v119, v109, vcc
	v_cndmask_b32_e64 v127, v127, v109, s[0:1]
	v_cndmask_b32_e64 v135, v135, v109, s[6:7]
	v_cndmask_b32_e64 v143, v143, v109, s[8:9]
	v_cmp_eq_u32_e32 vcc, v113, v8
	v_cmp_eq_u32_e64 s[0:1], v121, v8
	v_cmp_eq_u32_e64 s[6:7], v129, v8
	v_cmp_eq_u32_e64 s[8:9], v137, v8
	v_cndmask_b32_e32 v119, v119, v110, vcc
	v_cndmask_b32_e64 v127, v127, v110, s[0:1]
	v_cndmask_b32_e64 v135, v135, v110, s[6:7]
	v_cndmask_b32_e64 v143, v143, v110, s[8:9]
	v_cmp_eq_u32_e32 vcc, v113, v9
	v_cmp_eq_u32_e64 s[0:1], v121, v9
	v_cmp_eq_u32_e64 s[6:7], v129, v9
	v_cmp_eq_u32_e64 s[8:9], v137, v9
	v_cndmask_b32_e32 v119, v119, v111, vcc
	v_cndmask_b32_e64 v127, v127, v111, s[0:1]
	v_cndmask_b32_e64 v135, v135, v111, s[6:7]
	v_cndmask_b32_e64 v143, v143, v111, s[8:9]
.Lprep_a_m10:
	v_add_u32_e32 v112, v112, v119
	v_add_u32_e32 v120, v120, v127
	v_add_u32_e32 v128, v128, v135
	v_add_u32_e32 v136, v136, v143
	v_cmp_ne_u32_e32 vcc, -1, v119
	s_and_saveexec_b64 s[24:25], vcc
	ds_write_b32 v112, v114
	s_mov_b64 exec, s[24:25]
	v_cmp_ne_u32_e32 vcc, -1, v127
	s_and_saveexec_b64 s[24:25], vcc
	ds_write_b32 v120, v122
	s_mov_b64 exec, s[24:25]
	v_cmp_ne_u32_e32 vcc, -1, v135
	s_and_saveexec_b64 s[24:25], vcc
	ds_write_b32 v128, v130
	s_mov_b64 exec, s[24:25]
	v_cmp_ne_u32_e32 vcc, -1, v143
	s_and_saveexec_b64 s[24:25], vcc
	ds_write_b32 v136, v138
	s_mov_b64 exec, s[24:25]
	v_and_b32_e32 v112, 0xff, v84
	v_and_b32_e32 v120, 0xff, v85
	v_and_b32_e32 v128, 0xff, v86
	v_and_b32_e32 v136, 0xff, v87
	v_lshlrev_b32_e32 v112, 2, v112
	v_lshlrev_b32_e32 v120, 2, v120
	v_lshlrev_b32_e32 v128, 2, v128
	v_lshlrev_b32_e32 v136, 2, v136
	v_add_u32_e32 v118, v112, v11
	v_add_u32_e32 v126, v120, v11
	v_add_u32_e32 v134, v128, v11
	v_add_u32_e32 v142, v136, v11
	ds_read_b32 v113, v112 offset:36864
	ds_read_b32 v114, v112 offset:36224
	ds_read_b32 v115, v118 offset:22528
	ds_read_b32 v121, v120 offset:36864
	ds_read_b32 v122, v120 offset:36224
	ds_read_b32 v123, v126 offset:23040
	ds_read_b32 v129, v128 offset:36864
	ds_read_b32 v130, v128 offset:36224
	ds_read_b32 v131, v134 offset:23552
	ds_read_b32 v137, v136 offset:36864
	ds_read_b32 v138, v136 offset:36224
	ds_read_b32 v139, v142 offset:24064
	v_mov_b32_e32 v117, v37
	v_add_u32_e32 v37, 4, v37
	v_subrev_u32_e32 v118, s11, v37
	v_min_u32_e32 v37, v37, v118
	v_subrev_u32_e32 v118, s11, v37
	v_min_u32_e32 v37, v37, v118
	v_mov_b32_e32 v125, v37
	v_add_u32_e32 v37, 4, v37
	v_subrev_u32_e32 v126, s11, v37
	v_min_u32_e32 v37, v37, v126
	v_subrev_u32_e32 v126, s11, v37
	v_min_u32_e32 v37, v37, v126
	v_mov_b32_e32 v133, v37
	v_add_u32_e32 v37, 4, v37
	v_subrev_u32_e32 v134, s11, v37
	v_min_u32_e32 v37, v37, v134
	v_subrev_u32_e32 v134, s11, v37
	v_min_u32_e32 v37, v37, v134
	v_mov_b32_e32 v141, v37
	v_add_u32_e32 v37, 4, v37
	v_subrev_u32_e32 v142, s11, v37
	v_min_u32_e32 v37, v37, v142
	v_subrev_u32_e32 v142, s11, v37
	v_min_u32_e32 v37, v37, v142
	v_ashrrev_i32_e32 v116, 8, v84
	v_ashrrev_i32_e32 v124, 8, v85
	v_ashrrev_i32_e32 v132, 8, v86
	v_ashrrev_i32_e32 v140, 8, v87
	s_waitcnt lgkmcnt(0)
	v_add_u32_e32 v116, v116, v113
	v_add_u32_e32 v124, v124, v121
	v_add_u32_e32 v132, v132, v129
	v_add_u32_e32 v140, v140, v137
	v_add3_u32 v116, v116, v114, v115
	v_add3_u32 v124, v124, v122, v123
	v_add3_u32 v132, v132, v130, v131
	v_add3_u32 v140, v140, v138, v139
	v_cmp_eq_u32_e32 vcc, s93, v117
	v_add_u32_e32 v1, 0x16000, v10
	s_and_saveexec_b64 s[24:25], vcc
	global_store_dword v1, v116, s[16:17]
	s_mov_b64 exec, s[24:25]
	v_cmp_eq_u32_e32 vcc, s93, v125
	v_add_u32_e32 v1, 0x16800, v10
	s_and_saveexec_b64 s[24:25], vcc
	global_store_dword v1, v124, s[16:17]
	s_mov_b64 exec, s[24:25]
	v_cmp_eq_u32_e32 vcc, s93, v133
	v_add_u32_e32 v1, 0x17000, v10
	s_and_saveexec_b64 s[24:25], vcc
	global_store_dword v1, v132, s[16:17]
	s_mov_b64 exec, s[24:25]
	v_cmp_eq_u32_e32 vcc, s93, v141
	v_add_u32_e32 v1, 0x17800, v10
	s_and_saveexec_b64 s[24:25], vcc
	global_store_dword v1, v140, s[16:17]
	s_mov_b64 exec, s[24:25]
	v_ashrrev_i32_e32 v113, 8, v116
	v_ashrrev_i32_e32 v121, 8, v124
	v_ashrrev_i32_e32 v129, 8, v132
	v_ashrrev_i32_e32 v137, 8, v140
	v_and_b32_e32 v112, 0xff, v116
	v_and_b32_e32 v120, 0xff, v124
	v_and_b32_e32 v128, 0xff, v132
	v_and_b32_e32 v136, 0xff, v140
	v_lshl_add_u32 v112, v112, 2, s10
	v_lshl_add_u32 v120, v120, 2, s10
	v_lshl_add_u32 v128, v128, 2, s10
	v_lshl_add_u32 v136, v136, 2, s10
	v_add_u32_e32 v114, 0x2c00, v34
	v_add_u32_e32 v122, 0x2d00, v34
	v_add_u32_e32 v130, 0x2e00, v34
	v_add_u32_e32 v138, 0x2f00, v34
	v_mov_b32_e32 v119, -1
	v_mov_b32_e32 v127, -1
	v_mov_b32_e32 v135, -1
	v_mov_b32_e32 v143, -1
	v_cmp_eq_u32_e32 vcc, v113, v2
	v_cmp_eq_u32_e64 s[0:1], v121, v2
	v_cmp_eq_u32_e64 s[6:7], v129, v2
	v_cmp_eq_u32_e64 s[8:9], v137, v2
	v_cndmask_b32_e32 v119, v119, v104, vcc
	v_cndmask_b32_e64 v127, v127, v104, s[0:1]
	v_cndmask_b32_e64 v135, v135, v104, s[6:7]
	v_cndmask_b32_e64 v143, v143, v104, s[8:9]
	v_cmp_eq_u32_e32 vcc, v113, v3
	v_cmp_eq_u32_e64 s[0:1], v121, v3
	v_cmp_eq_u32_e64 s[6:7], v129, v3
	v_cmp_eq_u32_e64 s[8:9], v137, v3
	v_cndmask_b32_e32 v119, v119, v105, vcc
	v_cndmask_b32_e64 v127, v127, v105, s[0:1]
	v_cndmask_b32_e64 v135, v135, v105, s[6:7]
	v_cndmask_b32_e64 v143, v143, v105, s[8:9]
	v_cmp_eq_u32_e32 vcc, v113, v4
	v_cmp_eq_u32_e64 s[0:1], v121, v4
	v_cmp_eq_u32_e64 s[6:7], v129, v4
	v_cmp_eq_u32_e64 s[8:9], v137, v4
	v_cndmask_b32_e32 v119, v119, v106, vcc
	v_cndmask_b32_e64 v127, v127, v106, s[0:1]
	v_cndmask_b32_e64 v135, v135, v106, s[6:7]
	v_cndmask_b32_e64 v143, v143, v106, s[8:9]
	v_cmp_eq_u32_e32 vcc, v113, v5
	v_cmp_eq_u32_e64 s[0:1], v121, v5
	v_cmp_eq_u32_e64 s[6:7], v129, v5
	v_cmp_eq_u32_e64 s[8:9], v137, v5
	v_cndmask_b32_e32 v119, v119, v107, vcc
	v_cndmask_b32_e64 v127, v127, v107, s[0:1]
	v_cndmask_b32_e64 v135, v135, v107, s[6:7]
	v_cndmask_b32_e64 v143, v143, v107, s[8:9]
	v_cmp_gt_i32_e32 vcc, 0, v6
	s_cbranch_vccnz .Lprep_a_m11
	v_cmp_eq_u32_e32 vcc, v113, v6
	v_cmp_eq_u32_e64 s[0:1], v121, v6
	v_cmp_eq_u32_e64 s[6:7], v129, v6
	v_cmp_eq_u32_e64 s[8:9], v137, v6
	v_cndmask_b32_e32 v119, v119, v108, vcc
	v_cndmask_b32_e64 v127, v127, v108, s[0:1]
	v_cndmask_b32_e64 v135, v135, v108, s[6:7]
	v_cndmask_b32_e64 v143, v143, v108, s[8:9]
	v_cmp_eq_u32_e32 vcc, v113, v7
	v_cmp_eq_u32_e64 s[0:1], v121, v7
	v_cmp_eq_u32_e64 s[6:7], v129, v7
	v_cmp_eq_u32_e64 s[8:9], v137, v7
	v_cndmask_b32_e32 v119, v119, v109, vcc
	v_cndmask_b32_e64 v127, v127, v109, s[0:1]
	v_cndmask_b32_e64 v135, v135, v109, s[6:7]
	v_cndmask_b32_e64 v143, v143, v109, s[8:9]
	v_cmp_eq_u32_e32 vcc, v113, v8
	v_cmp_eq_u32_e64 s[0:1], v121, v8
	v_cmp_eq_u32_e64 s[6:7], v129, v8
	v_cmp_eq_u32_e64 s[8:9], v137, v8
	v_cndmask_b32_e32 v119, v119, v110, vcc
	v_cndmask_b32_e64 v127, v127, v110, s[0:1]
	v_cndmask_b32_e64 v135, v135, v110, s[6:7]
	v_cndmask_b32_e64 v143, v143, v110, s[8:9]
	v_cmp_eq_u32_e32 vcc, v113, v9
	v_cmp_eq_u32_e64 s[0:1], v121, v9
	v_cmp_eq_u32_e64 s[6:7], v129, v9
	v_cmp_eq_u32_e64 s[8:9], v137, v9
	v_cndmask_b32_e32 v119, v119, v111, vcc
	v_cndmask_b32_e64 v127, v127, v111, s[0:1]
	v_cndmask_b32_e64 v135, v135, v111, s[6:7]
	v_cndmask_b32_e64 v143, v143, v111, s[8:9]
.Lprep_a_m11:
	v_add_u32_e32 v112, v112, v119
	v_add_u32_e32 v120, v120, v127
	v_add_u32_e32 v128, v128, v135
	v_add_u32_e32 v136, v136, v143
	v_cmp_ne_u32_e32 vcc, -1, v119
	s_and_saveexec_b64 s[24:25], vcc
	ds_write_b32 v112, v114
	s_mov_b64 exec, s[24:25]
	v_cmp_ne_u32_e32 vcc, -1, v127
	s_and_saveexec_b64 s[24:25], vcc
	ds_write_b32 v120, v122
	s_mov_b64 exec, s[24:25]
	v_cmp_ne_u32_e32 vcc, -1, v135
	s_and_saveexec_b64 s[24:25], vcc
	ds_write_b32 v128, v130
	s_mov_b64 exec, s[24:25]
	v_cmp_ne_u32_e32 vcc, -1, v143
	s_and_saveexec_b64 s[24:25], vcc
	ds_write_b32 v136, v138
	s_mov_b64 exec, s[24:25]
	v_and_b32_e32 v112, 0xff, v88
	v_and_b32_e32 v120, 0xff, v89
	v_and_b32_e32 v128, 0xff, v90
	v_and_b32_e32 v136, 0xff, v91
	v_lshlrev_b32_e32 v112, 2, v112
	v_lshlrev_b32_e32 v120, 2, v120
	v_lshlrev_b32_e32 v128, 2, v128
	v_lshlrev_b32_e32 v136, 2, v136
	v_add_u32_e32 v118, v112, v11
	v_add_u32_e32 v126, v120, v11
	v_add_u32_e32 v134, v128, v11
	v_add_u32_e32 v142, v136, v11
	ds_read_b32 v113, v112 offset:36864
	ds_read_b32 v114, v112 offset:36352
	ds_read_b32 v115, v118 offset:24576
	ds_read_b32 v121, v120 offset:36864
	ds_read_b32 v122, v120 offset:36352
	ds_read_b32 v123, v126 offset:25088
	ds_read_b32 v129, v128 offset:36864
	ds_read_b32 v130, v128 offset:36352
	ds_read_b32 v131, v134 offset:25600
	ds_read_b32 v137, v136 offset:36864
	ds_read_b32 v138, v136 offset:36352
	ds_read_b32 v139, v142 offset:26112
	v_mov_b32_e32 v117, v37
	v_add_u32_e32 v37, 4, v37
	v_subrev_u32_e32 v118, s11, v37
	v_min_u32_e32 v37, v37, v118
	v_subrev_u32_e32 v118, s11, v37
	v_min_u32_e32 v37, v37, v118
	v_mov_b32_e32 v125, v37
	v_add_u32_e32 v37, 4, v37
	v_subrev_u32_e32 v126, s11, v37
	v_min_u32_e32 v37, v37, v126
	v_subrev_u32_e32 v126, s11, v37
	v_min_u32_e32 v37, v37, v126
	v_mov_b32_e32 v133, v37
	v_add_u32_e32 v37, 4, v37
	v_subrev_u32_e32 v134, s11, v37
	v_min_u32_e32 v37, v37, v134
	v_subrev_u32_e32 v134, s11, v37
	v_min_u32_e32 v37, v37, v134
	v_mov_b32_e32 v141, v37
	v_add_u32_e32 v37, 4, v37
	v_subrev_u32_e32 v142, s11, v37
	v_min_u32_e32 v37, v37, v142
	v_subrev_u32_e32 v142, s11, v37
	v_min_u32_e32 v37, v37, v142
	v_ashrrev_i32_e32 v116, 8, v88
	v_ashrrev_i32_e32 v124, 8, v89
	v_ashrrev_i32_e32 v132, 8, v90
	v_ashrrev_i32_e32 v140, 8, v91
	s_waitcnt lgkmcnt(0)
	v_add_u32_e32 v116, v116, v113
	v_add_u32_e32 v124, v124, v121
	v_add_u32_e32 v132, v132, v129
	v_add_u32_e32 v140, v140, v137
	v_add3_u32 v116, v116, v114, v115
	v_add3_u32 v124, v124, v122, v123
	v_add3_u32 v132, v132, v130, v131
	v_add3_u32 v140, v140, v138, v139
	v_cmp_eq_u32_e32 vcc, s93, v117
	v_add_u32_e32 v1, 0x18000, v10
	s_and_saveexec_b64 s[24:25], vcc
	global_store_dword v1, v116, s[16:17]
	s_mov_b64 exec, s[24:25]
	v_cmp_eq_u32_e32 vcc, s93, v125
	v_add_u32_e32 v1, 0x18800, v10
	s_and_saveexec_b64 s[24:25], vcc
	global_store_dword v1, v124, s[16:17]
	s_mov_b64 exec, s[24:25]
	v_cmp_eq_u32_e32 vcc, s93, v133
	v_add_u32_e32 v1, 0x19000, v10
	s_and_saveexec_b64 s[24:25], vcc
	global_store_dword v1, v132, s[16:17]
	s_mov_b64 exec, s[24:25]
	v_cmp_eq_u32_e32 vcc, s93, v141
	v_add_u32_e32 v1, 0x19800, v10
	s_and_saveexec_b64 s[24:25], vcc
	global_store_dword v1, v140, s[16:17]
	s_mov_b64 exec, s[24:25]
	v_ashrrev_i32_e32 v113, 8, v116
	v_ashrrev_i32_e32 v121, 8, v124
	v_ashrrev_i32_e32 v129, 8, v132
	v_ashrrev_i32_e32 v137, 8, v140
	v_and_b32_e32 v112, 0xff, v116
	v_and_b32_e32 v120, 0xff, v124
	v_and_b32_e32 v128, 0xff, v132
	v_and_b32_e32 v136, 0xff, v140
	v_lshl_add_u32 v112, v112, 2, s10
	v_lshl_add_u32 v120, v120, 2, s10
	v_lshl_add_u32 v128, v128, 2, s10
	v_lshl_add_u32 v136, v136, 2, s10
	v_add_u32_e32 v114, 0x3000, v34
	v_add_u32_e32 v122, 0x3100, v34
	v_add_u32_e32 v130, 0x3200, v34
	v_add_u32_e32 v138, 0x3300, v34
	v_mov_b32_e32 v119, -1
	v_mov_b32_e32 v127, -1
	v_mov_b32_e32 v135, -1
	v_mov_b32_e32 v143, -1
	v_cmp_eq_u32_e32 vcc, v113, v2
	v_cmp_eq_u32_e64 s[0:1], v121, v2
	v_cmp_eq_u32_e64 s[6:7], v129, v2
	v_cmp_eq_u32_e64 s[8:9], v137, v2
	v_cndmask_b32_e32 v119, v119, v104, vcc
	v_cndmask_b32_e64 v127, v127, v104, s[0:1]
	v_cndmask_b32_e64 v135, v135, v104, s[6:7]
	v_cndmask_b32_e64 v143, v143, v104, s[8:9]
	v_cmp_eq_u32_e32 vcc, v113, v3
	v_cmp_eq_u32_e64 s[0:1], v121, v3
	v_cmp_eq_u32_e64 s[6:7], v129, v3
	v_cmp_eq_u32_e64 s[8:9], v137, v3
	v_cndmask_b32_e32 v119, v119, v105, vcc
	v_cndmask_b32_e64 v127, v127, v105, s[0:1]
	v_cndmask_b32_e64 v135, v135, v105, s[6:7]
	v_cndmask_b32_e64 v143, v143, v105, s[8:9]
	v_cmp_eq_u32_e32 vcc, v113, v4
	v_cmp_eq_u32_e64 s[0:1], v121, v4
	v_cmp_eq_u32_e64 s[6:7], v129, v4
	v_cmp_eq_u32_e64 s[8:9], v137, v4
	v_cndmask_b32_e32 v119, v119, v106, vcc
	v_cndmask_b32_e64 v127, v127, v106, s[0:1]
	v_cndmask_b32_e64 v135, v135, v106, s[6:7]
	v_cndmask_b32_e64 v143, v143, v106, s[8:9]
	v_cmp_eq_u32_e32 vcc, v113, v5
	v_cmp_eq_u32_e64 s[0:1], v121, v5
	v_cmp_eq_u32_e64 s[6:7], v129, v5
	v_cmp_eq_u32_e64 s[8:9], v137, v5
	v_cndmask_b32_e32 v119, v119, v107, vcc
	v_cndmask_b32_e64 v127, v127, v107, s[0:1]
	v_cndmask_b32_e64 v135, v135, v107, s[6:7]
	v_cndmask_b32_e64 v143, v143, v107, s[8:9]
	v_cmp_gt_i32_e32 vcc, 0, v6
	s_cbranch_vccnz .Lprep_a_m12
	v_cmp_eq_u32_e32 vcc, v113, v6
	v_cmp_eq_u32_e64 s[0:1], v121, v6
	v_cmp_eq_u32_e64 s[6:7], v129, v6
	v_cmp_eq_u32_e64 s[8:9], v137, v6
	v_cndmask_b32_e32 v119, v119, v108, vcc
	v_cndmask_b32_e64 v127, v127, v108, s[0:1]
	v_cndmask_b32_e64 v135, v135, v108, s[6:7]
	v_cndmask_b32_e64 v143, v143, v108, s[8:9]
	v_cmp_eq_u32_e32 vcc, v113, v7
	v_cmp_eq_u32_e64 s[0:1], v121, v7
	v_cmp_eq_u32_e64 s[6:7], v129, v7
	v_cmp_eq_u32_e64 s[8:9], v137, v7
	v_cndmask_b32_e32 v119, v119, v109, vcc
	v_cndmask_b32_e64 v127, v127, v109, s[0:1]
	v_cndmask_b32_e64 v135, v135, v109, s[6:7]
	v_cndmask_b32_e64 v143, v143, v109, s[8:9]
	v_cmp_eq_u32_e32 vcc, v113, v8
	v_cmp_eq_u32_e64 s[0:1], v121, v8
	v_cmp_eq_u32_e64 s[6:7], v129, v8
	v_cmp_eq_u32_e64 s[8:9], v137, v8
	v_cndmask_b32_e32 v119, v119, v110, vcc
	v_cndmask_b32_e64 v127, v127, v110, s[0:1]
	v_cndmask_b32_e64 v135, v135, v110, s[6:7]
	v_cndmask_b32_e64 v143, v143, v110, s[8:9]
	v_cmp_eq_u32_e32 vcc, v113, v9
	v_cmp_eq_u32_e64 s[0:1], v121, v9
	v_cmp_eq_u32_e64 s[6:7], v129, v9
	v_cmp_eq_u32_e64 s[8:9], v137, v9
	v_cndmask_b32_e32 v119, v119, v111, vcc
	v_cndmask_b32_e64 v127, v127, v111, s[0:1]
	v_cndmask_b32_e64 v135, v135, v111, s[6:7]
	v_cndmask_b32_e64 v143, v143, v111, s[8:9]
.Lprep_a_m12:
	v_add_u32_e32 v112, v112, v119
	v_add_u32_e32 v120, v120, v127
	v_add_u32_e32 v128, v128, v135
	v_add_u32_e32 v136, v136, v143
	v_cmp_ne_u32_e32 vcc, -1, v119
	s_and_saveexec_b64 s[24:25], vcc
	ds_write_b32 v112, v114
	s_mov_b64 exec, s[24:25]
	v_cmp_ne_u32_e32 vcc, -1, v127
	s_and_saveexec_b64 s[24:25], vcc
	ds_write_b32 v120, v122
	s_mov_b64 exec, s[24:25]
	v_cmp_ne_u32_e32 vcc, -1, v135
	s_and_saveexec_b64 s[24:25], vcc
	ds_write_b32 v128, v130
	s_mov_b64 exec, s[24:25]
	v_cmp_ne_u32_e32 vcc, -1, v143
	s_and_saveexec_b64 s[24:25], vcc
	ds_write_b32 v136, v138
	s_mov_b64 exec, s[24:25]
	v_and_b32_e32 v112, 0xff, v92
	v_and_b32_e32 v120, 0xff, v93
	v_and_b32_e32 v128, 0xff, v94
	v_and_b32_e32 v136, 0xff, v95
	v_lshlrev_b32_e32 v112, 2, v112
	v_lshlrev_b32_e32 v120, 2, v120
	v_lshlrev_b32_e32 v128, 2, v128
	v_lshlrev_b32_e32 v136, 2, v136
	v_add_u32_e32 v118, v112, v11
	v_add_u32_e32 v126, v120, v11
	v_add_u32_e32 v134, v128, v11
	v_add_u32_e32 v142, v136, v11
	ds_read_b32 v113, v112 offset:36864
	ds_read_b32 v114, v112 offset:36480
	ds_read_b32 v115, v118 offset:26624
	ds_read_b32 v121, v120 offset:36864
	ds_read_b32 v122, v120 offset:36480
	ds_read_b32 v123, v126 offset:27136
	ds_read_b32 v129, v128 offset:36864
	ds_read_b32 v130, v128 offset:36480
	ds_read_b32 v131, v134 offset:27648
	ds_read_b32 v137, v136 offset:36864
	ds_read_b32 v138, v136 offset:36480
	ds_read_b32 v139, v142 offset:28160
	v_mov_b32_e32 v117, v37
	v_add_u32_e32 v37, 4, v37
	v_subrev_u32_e32 v118, s11, v37
	v_min_u32_e32 v37, v37, v118
	v_subrev_u32_e32 v118, s11, v37
	v_min_u32_e32 v37, v37, v118
	v_mov_b32_e32 v125, v37
	v_add_u32_e32 v37, 4, v37
	v_subrev_u32_e32 v126, s11, v37
	v_min_u32_e32 v37, v37, v126
	v_subrev_u32_e32 v126, s11, v37
	v_min_u32_e32 v37, v37, v126
	v_mov_b32_e32 v133, v37
	v_add_u32_e32 v37, 4, v37
	v_subrev_u32_e32 v134, s11, v37
	v_min_u32_e32 v37, v37, v134
	v_subrev_u32_e32 v134, s11, v37
	v_min_u32_e32 v37, v37, v134
	v_mov_b32_e32 v141, v37
	v_add_u32_e32 v37, 4, v37
	v_subrev_u32_e32 v142, s11, v37
	v_min_u32_e32 v37, v37, v142
	v_subrev_u32_e32 v142, s11, v37
	v_min_u32_e32 v37, v37, v142
	v_ashrrev_i32_e32 v116, 8, v92
	v_ashrrev_i32_e32 v124, 8, v93
	v_ashrrev_i32_e32 v132, 8, v94
	v_ashrrev_i32_e32 v140, 8, v95
	s_waitcnt lgkmcnt(0)
	v_add_u32_e32 v116, v116, v113
	v_add_u32_e32 v124, v124, v121
	v_add_u32_e32 v132, v132, v129
	v_add_u32_e32 v140, v140, v137
	v_add3_u32 v116, v116, v114, v115
	v_add3_u32 v124, v124, v122, v123
	v_add3_u32 v132, v132, v130, v131
	v_add3_u32 v140, v140, v138, v139
	v_cmp_eq_u32_e32 vcc, s93, v117
	v_add_u32_e32 v1, 0x1a000, v10
	s_and_saveexec_b64 s[24:25], vcc
	global_store_dword v1, v116, s[16:17]
	s_mov_b64 exec, s[24:25]
	v_cmp_eq_u32_e32 vcc, s93, v125
	v_add_u32_e32 v1, 0x1a800, v10
	s_and_saveexec_b64 s[24:25], vcc
	global_store_dword v1, v124, s[16:17]
	s_mov_b64 exec, s[24:25]
	v_cmp_eq_u32_e32 vcc, s93, v133
	v_add_u32_e32 v1, 0x1b000, v10
	s_and_saveexec_b64 s[24:25], vcc
	global_store_dword v1, v132, s[16:17]
	s_mov_b64 exec, s[24:25]
	v_cmp_eq_u32_e32 vcc, s93, v141
	v_add_u32_e32 v1, 0x1b800, v10
	s_and_saveexec_b64 s[24:25], vcc
	global_store_dword v1, v140, s[16:17]
	s_mov_b64 exec, s[24:25]
	v_ashrrev_i32_e32 v113, 8, v116
	v_ashrrev_i32_e32 v121, 8, v124
	v_ashrrev_i32_e32 v129, 8, v132
	v_ashrrev_i32_e32 v137, 8, v140
	v_and_b32_e32 v112, 0xff, v116
	v_and_b32_e32 v120, 0xff, v124
	v_and_b32_e32 v128, 0xff, v132
	v_and_b32_e32 v136, 0xff, v140
	v_lshl_add_u32 v112, v112, 2, s10
	v_lshl_add_u32 v120, v120, 2, s10
	v_lshl_add_u32 v128, v128, 2, s10
	v_lshl_add_u32 v136, v136, 2, s10
	v_add_u32_e32 v114, 0x3400, v34
	v_add_u32_e32 v122, 0x3500, v34
	v_add_u32_e32 v130, 0x3600, v34
	v_add_u32_e32 v138, 0x3700, v34
	v_mov_b32_e32 v119, -1
	v_mov_b32_e32 v127, -1
	v_mov_b32_e32 v135, -1
	v_mov_b32_e32 v143, -1
	v_cmp_eq_u32_e32 vcc, v113, v2
	v_cmp_eq_u32_e64 s[0:1], v121, v2
	v_cmp_eq_u32_e64 s[6:7], v129, v2
	v_cmp_eq_u32_e64 s[8:9], v137, v2
	v_cndmask_b32_e32 v119, v119, v104, vcc
	v_cndmask_b32_e64 v127, v127, v104, s[0:1]
	v_cndmask_b32_e64 v135, v135, v104, s[6:7]
	v_cndmask_b32_e64 v143, v143, v104, s[8:9]
	v_cmp_eq_u32_e32 vcc, v113, v3
	v_cmp_eq_u32_e64 s[0:1], v121, v3
	v_cmp_eq_u32_e64 s[6:7], v129, v3
	v_cmp_eq_u32_e64 s[8:9], v137, v3
	v_cndmask_b32_e32 v119, v119, v105, vcc
	v_cndmask_b32_e64 v127, v127, v105, s[0:1]
	v_cndmask_b32_e64 v135, v135, v105, s[6:7]
	v_cndmask_b32_e64 v143, v143, v105, s[8:9]
	v_cmp_eq_u32_e32 vcc, v113, v4
	v_cmp_eq_u32_e64 s[0:1], v121, v4
	v_cmp_eq_u32_e64 s[6:7], v129, v4
	v_cmp_eq_u32_e64 s[8:9], v137, v4
	v_cndmask_b32_e32 v119, v119, v106, vcc
	v_cndmask_b32_e64 v127, v127, v106, s[0:1]
	v_cndmask_b32_e64 v135, v135, v106, s[6:7]
	v_cndmask_b32_e64 v143, v143, v106, s[8:9]
	v_cmp_eq_u32_e32 vcc, v113, v5
	v_cmp_eq_u32_e64 s[0:1], v121, v5
	v_cmp_eq_u32_e64 s[6:7], v129, v5
	v_cmp_eq_u32_e64 s[8:9], v137, v5
	v_cndmask_b32_e32 v119, v119, v107, vcc
	v_cndmask_b32_e64 v127, v127, v107, s[0:1]
	v_cndmask_b32_e64 v135, v135, v107, s[6:7]
	v_cndmask_b32_e64 v143, v143, v107, s[8:9]
	v_cmp_gt_i32_e32 vcc, 0, v6
	s_cbranch_vccnz .Lprep_a_m13
	v_cmp_eq_u32_e32 vcc, v113, v6
	v_cmp_eq_u32_e64 s[0:1], v121, v6
	v_cmp_eq_u32_e64 s[6:7], v129, v6
	v_cmp_eq_u32_e64 s[8:9], v137, v6
	v_cndmask_b32_e32 v119, v119, v108, vcc
	v_cndmask_b32_e64 v127, v127, v108, s[0:1]
	v_cndmask_b32_e64 v135, v135, v108, s[6:7]
	v_cndmask_b32_e64 v143, v143, v108, s[8:9]
	v_cmp_eq_u32_e32 vcc, v113, v7
	v_cmp_eq_u32_e64 s[0:1], v121, v7
	v_cmp_eq_u32_e64 s[6:7], v129, v7
	v_cmp_eq_u32_e64 s[8:9], v137, v7
	v_cndmask_b32_e32 v119, v119, v109, vcc
	v_cndmask_b32_e64 v127, v127, v109, s[0:1]
	v_cndmask_b32_e64 v135, v135, v109, s[6:7]
	v_cndmask_b32_e64 v143, v143, v109, s[8:9]
	v_cmp_eq_u32_e32 vcc, v113, v8
	v_cmp_eq_u32_e64 s[0:1], v121, v8
	v_cmp_eq_u32_e64 s[6:7], v129, v8
	v_cmp_eq_u32_e64 s[8:9], v137, v8
	v_cndmask_b32_e32 v119, v119, v110, vcc
	v_cndmask_b32_e64 v127, v127, v110, s[0:1]
	v_cndmask_b32_e64 v135, v135, v110, s[6:7]
	v_cndmask_b32_e64 v143, v143, v110, s[8:9]
	v_cmp_eq_u32_e32 vcc, v113, v9
	v_cmp_eq_u32_e64 s[0:1], v121, v9
	v_cmp_eq_u32_e64 s[6:7], v129, v9
	v_cmp_eq_u32_e64 s[8:9], v137, v9
	v_cndmask_b32_e32 v119, v119, v111, vcc
	v_cndmask_b32_e64 v127, v127, v111, s[0:1]
	v_cndmask_b32_e64 v135, v135, v111, s[6:7]
	v_cndmask_b32_e64 v143, v143, v111, s[8:9]
.Lprep_a_m13:
	v_add_u32_e32 v112, v112, v119
	v_add_u32_e32 v120, v120, v127
	v_add_u32_e32 v128, v128, v135
	v_add_u32_e32 v136, v136, v143
	v_cmp_ne_u32_e32 vcc, -1, v119
	s_and_saveexec_b64 s[24:25], vcc
	ds_write_b32 v112, v114
	s_mov_b64 exec, s[24:25]
	v_cmp_ne_u32_e32 vcc, -1, v127
	s_and_saveexec_b64 s[24:25], vcc
	ds_write_b32 v120, v122
	s_mov_b64 exec, s[24:25]
	v_cmp_ne_u32_e32 vcc, -1, v135
	s_and_saveexec_b64 s[24:25], vcc
	ds_write_b32 v128, v130
	s_mov_b64 exec, s[24:25]
	v_cmp_ne_u32_e32 vcc, -1, v143
	s_and_saveexec_b64 s[24:25], vcc
	ds_write_b32 v136, v138
	s_mov_b64 exec, s[24:25]
	v_and_b32_e32 v112, 0xff, v96
	v_and_b32_e32 v120, 0xff, v97
	v_and_b32_e32 v128, 0xff, v98
	v_and_b32_e32 v136, 0xff, v99
	v_lshlrev_b32_e32 v112, 2, v112
	v_lshlrev_b32_e32 v120, 2, v120
	v_lshlrev_b32_e32 v128, 2, v128
	v_lshlrev_b32_e32 v136, 2, v136
	v_add_u32_e32 v118, v112, v11
	v_add_u32_e32 v126, v120, v11
	v_add_u32_e32 v134, v128, v11
	v_add_u32_e32 v142, v136, v11
	ds_read_b32 v113, v112 offset:36864
	ds_read_b32 v114, v112 offset:36608
	ds_read_b32 v115, v118 offset:28672
	ds_read_b32 v121, v120 offset:36864
	ds_read_b32 v122, v120 offset:36608
	ds_read_b32 v123, v126 offset:29184
	ds_read_b32 v129, v128 offset:36864
	ds_read_b32 v130, v128 offset:36608
	ds_read_b32 v131, v134 offset:29696
	ds_read_b32 v137, v136 offset:36864
	ds_read_b32 v138, v136 offset:36608
	ds_read_b32 v139, v142 offset:30208
	v_mov_b32_e32 v117, v37
	v_add_u32_e32 v37, 4, v37
	v_subrev_u32_e32 v118, s11, v37
	v_min_u32_e32 v37, v37, v118
	v_subrev_u32_e32 v118, s11, v37
	v_min_u32_e32 v37, v37, v118
	v_mov_b32_e32 v125, v37
	v_add_u32_e32 v37, 4, v37
	v_subrev_u32_e32 v126, s11, v37
	v_min_u32_e32 v37, v37, v126
	v_subrev_u32_e32 v126, s11, v37
	v_min_u32_e32 v37, v37, v126
	v_mov_b32_e32 v133, v37
	v_add_u32_e32 v37, 4, v37
	v_subrev_u32_e32 v134, s11, v37
	v_min_u32_e32 v37, v37, v134
	v_subrev_u32_e32 v134, s11, v37
	v_min_u32_e32 v37, v37, v134
	v_mov_b32_e32 v141, v37
	v_add_u32_e32 v37, 4, v37
	v_subrev_u32_e32 v142, s11, v37
	v_min_u32_e32 v37, v37, v142
	v_subrev_u32_e32 v142, s11, v37
	v_min_u32_e32 v37, v37, v142
	v_ashrrev_i32_e32 v116, 8, v96
	v_ashrrev_i32_e32 v124, 8, v97
	v_ashrrev_i32_e32 v132, 8, v98
	v_ashrrev_i32_e32 v140, 8, v99
	s_waitcnt lgkmcnt(0)
	v_add_u32_e32 v116, v116, v113
	v_add_u32_e32 v124, v124, v121
	v_add_u32_e32 v132, v132, v129
	v_add_u32_e32 v140, v140, v137
	v_add3_u32 v116, v116, v114, v115
	v_add3_u32 v124, v124, v122, v123
	v_add3_u32 v132, v132, v130, v131
	v_add3_u32 v140, v140, v138, v139
	v_cmp_eq_u32_e32 vcc, s93, v117
	v_add_u32_e32 v1, 0x1c000, v10
	s_and_saveexec_b64 s[24:25], vcc
	global_store_dword v1, v116, s[16:17]
	s_mov_b64 exec, s[24:25]
	v_cmp_eq_u32_e32 vcc, s93, v125
	v_add_u32_e32 v1, 0x1c800, v10
	s_and_saveexec_b64 s[24:25], vcc
	global_store_dword v1, v124, s[16:17]
	s_mov_b64 exec, s[24:25]
	v_cmp_eq_u32_e32 vcc, s93, v133
	v_add_u32_e32 v1, 0x1d000, v10
	s_and_saveexec_b64 s[24:25], vcc
	global_store_dword v1, v132, s[16:17]
	s_mov_b64 exec, s[24:25]
	v_cmp_eq_u32_e32 vcc, s93, v141
	v_add_u32_e32 v1, 0x1d800, v10
	s_and_saveexec_b64 s[24:25], vcc
	global_store_dword v1, v140, s[16:17]
	s_mov_b64 exec, s[24:25]
	v_ashrrev_i32_e32 v113, 8, v116
	v_ashrrev_i32_e32 v121, 8, v124
	v_ashrrev_i32_e32 v129, 8, v132
	v_ashrrev_i32_e32 v137, 8, v140
	v_and_b32_e32 v112, 0xff, v116
	v_and_b32_e32 v120, 0xff, v124
	v_and_b32_e32 v128, 0xff, v132
	v_and_b32_e32 v136, 0xff, v140
	v_lshl_add_u32 v112, v112, 2, s10
	v_lshl_add_u32 v120, v120, 2, s10
	v_lshl_add_u32 v128, v128, 2, s10
	v_lshl_add_u32 v136, v136, 2, s10
	v_add_u32_e32 v114, 0x3800, v34
	v_add_u32_e32 v122, 0x3900, v34
	v_add_u32_e32 v130, 0x3a00, v34
	v_add_u32_e32 v138, 0x3b00, v34
	v_mov_b32_e32 v119, -1
	v_mov_b32_e32 v127, -1
	v_mov_b32_e32 v135, -1
	v_mov_b32_e32 v143, -1
	v_cmp_eq_u32_e32 vcc, v113, v2
	v_cmp_eq_u32_e64 s[0:1], v121, v2
	v_cmp_eq_u32_e64 s[6:7], v129, v2
	v_cmp_eq_u32_e64 s[8:9], v137, v2
	v_cndmask_b32_e32 v119, v119, v104, vcc
	v_cndmask_b32_e64 v127, v127, v104, s[0:1]
	v_cndmask_b32_e64 v135, v135, v104, s[6:7]
	v_cndmask_b32_e64 v143, v143, v104, s[8:9]
	v_cmp_eq_u32_e32 vcc, v113, v3
	v_cmp_eq_u32_e64 s[0:1], v121, v3
	v_cmp_eq_u32_e64 s[6:7], v129, v3
	v_cmp_eq_u32_e64 s[8:9], v137, v3
	v_cndmask_b32_e32 v119, v119, v105, vcc
	v_cndmask_b32_e64 v127, v127, v105, s[0:1]
	v_cndmask_b32_e64 v135, v135, v105, s[6:7]
	v_cndmask_b32_e64 v143, v143, v105, s[8:9]
	v_cmp_eq_u32_e32 vcc, v113, v4
	v_cmp_eq_u32_e64 s[0:1], v121, v4
	v_cmp_eq_u32_e64 s[6:7], v129, v4
	v_cmp_eq_u32_e64 s[8:9], v137, v4
	v_cndmask_b32_e32 v119, v119, v106, vcc
	v_cndmask_b32_e64 v127, v127, v106, s[0:1]
	v_cndmask_b32_e64 v135, v135, v106, s[6:7]
	v_cndmask_b32_e64 v143, v143, v106, s[8:9]
	v_cmp_eq_u32_e32 vcc, v113, v5
	v_cmp_eq_u32_e64 s[0:1], v121, v5
	v_cmp_eq_u32_e64 s[6:7], v129, v5
	v_cmp_eq_u32_e64 s[8:9], v137, v5
	v_cndmask_b32_e32 v119, v119, v107, vcc
	v_cndmask_b32_e64 v127, v127, v107, s[0:1]
	v_cndmask_b32_e64 v135, v135, v107, s[6:7]
	v_cndmask_b32_e64 v143, v143, v107, s[8:9]
	v_cmp_gt_i32_e32 vcc, 0, v6
	s_cbranch_vccnz .Lprep_a_m14
	v_cmp_eq_u32_e32 vcc, v113, v6
	v_cmp_eq_u32_e64 s[0:1], v121, v6
	v_cmp_eq_u32_e64 s[6:7], v129, v6
	v_cmp_eq_u32_e64 s[8:9], v137, v6
	v_cndmask_b32_e32 v119, v119, v108, vcc
	v_cndmask_b32_e64 v127, v127, v108, s[0:1]
	v_cndmask_b32_e64 v135, v135, v108, s[6:7]
	v_cndmask_b32_e64 v143, v143, v108, s[8:9]
	v_cmp_eq_u32_e32 vcc, v113, v7
	v_cmp_eq_u32_e64 s[0:1], v121, v7
	v_cmp_eq_u32_e64 s[6:7], v129, v7
	v_cmp_eq_u32_e64 s[8:9], v137, v7
	v_cndmask_b32_e32 v119, v119, v109, vcc
	v_cndmask_b32_e64 v127, v127, v109, s[0:1]
	v_cndmask_b32_e64 v135, v135, v109, s[6:7]
	v_cndmask_b32_e64 v143, v143, v109, s[8:9]
	v_cmp_eq_u32_e32 vcc, v113, v8
	v_cmp_eq_u32_e64 s[0:1], v121, v8
	v_cmp_eq_u32_e64 s[6:7], v129, v8
	v_cmp_eq_u32_e64 s[8:9], v137, v8
	v_cndmask_b32_e32 v119, v119, v110, vcc
	v_cndmask_b32_e64 v127, v127, v110, s[0:1]
	v_cndmask_b32_e64 v135, v135, v110, s[6:7]
	v_cndmask_b32_e64 v143, v143, v110, s[8:9]
	v_cmp_eq_u32_e32 vcc, v113, v9
	v_cmp_eq_u32_e64 s[0:1], v121, v9
	v_cmp_eq_u32_e64 s[6:7], v129, v9
	v_cmp_eq_u32_e64 s[8:9], v137, v9
	v_cndmask_b32_e32 v119, v119, v111, vcc
	v_cndmask_b32_e64 v127, v127, v111, s[0:1]
	v_cndmask_b32_e64 v135, v135, v111, s[6:7]
	v_cndmask_b32_e64 v143, v143, v111, s[8:9]
.Lprep_a_m14:
	v_add_u32_e32 v112, v112, v119
	v_add_u32_e32 v120, v120, v127
	v_add_u32_e32 v128, v128, v135
	v_add_u32_e32 v136, v136, v143
	v_cmp_ne_u32_e32 vcc, -1, v119
	s_and_saveexec_b64 s[24:25], vcc
	ds_write_b32 v112, v114
	s_mov_b64 exec, s[24:25]
	v_cmp_ne_u32_e32 vcc, -1, v127
	s_and_saveexec_b64 s[24:25], vcc
	ds_write_b32 v120, v122
	s_mov_b64 exec, s[24:25]
	v_cmp_ne_u32_e32 vcc, -1, v135
	s_and_saveexec_b64 s[24:25], vcc
	ds_write_b32 v128, v130
	s_mov_b64 exec, s[24:25]
	v_cmp_ne_u32_e32 vcc, -1, v143
	s_and_saveexec_b64 s[24:25], vcc
	ds_write_b32 v136, v138
	s_mov_b64 exec, s[24:25]
	v_and_b32_e32 v112, 0xff, v100
	v_and_b32_e32 v120, 0xff, v101
	v_and_b32_e32 v128, 0xff, v102
	v_and_b32_e32 v136, 0xff, v103
	v_lshlrev_b32_e32 v112, 2, v112
	v_lshlrev_b32_e32 v120, 2, v120
	v_lshlrev_b32_e32 v128, 2, v128
	v_lshlrev_b32_e32 v136, 2, v136
	v_add_u32_e32 v118, v112, v11
	v_add_u32_e32 v126, v120, v11
	v_add_u32_e32 v134, v128, v11
	v_add_u32_e32 v142, v136, v11
	ds_read_b32 v113, v112 offset:36864
	ds_read_b32 v114, v112 offset:36736
	ds_read_b32 v115, v118 offset:30720
	ds_read_b32 v121, v120 offset:36864
	ds_read_b32 v122, v120 offset:36736
	ds_read_b32 v123, v126 offset:31232
	ds_read_b32 v129, v128 offset:36864
	ds_read_b32 v130, v128 offset:36736
	ds_read_b32 v131, v134 offset:31744
	ds_read_b32 v137, v136 offset:36864
	ds_read_b32 v138, v136 offset:36736
	ds_read_b32 v139, v142 offset:32256
	v_mov_b32_e32 v117, v37
	v_add_u32_e32 v37, 4, v37
	v_subrev_u32_e32 v118, s11, v37
	v_min_u32_e32 v37, v37, v118
	v_subrev_u32_e32 v118, s11, v37
	v_min_u32_e32 v37, v37, v118
	v_mov_b32_e32 v125, v37
	v_add_u32_e32 v37, 4, v37
	v_subrev_u32_e32 v126, s11, v37
	v_min_u32_e32 v37, v37, v126
	v_subrev_u32_e32 v126, s11, v37
	v_min_u32_e32 v37, v37, v126
	v_mov_b32_e32 v133, v37
	v_add_u32_e32 v37, 4, v37
	v_subrev_u32_e32 v134, s11, v37
	v_min_u32_e32 v37, v37, v134
	v_subrev_u32_e32 v134, s11, v37
	v_min_u32_e32 v37, v37, v134
	v_mov_b32_e32 v141, v37
	v_add_u32_e32 v37, 4, v37
	v_subrev_u32_e32 v142, s11, v37
	v_min_u32_e32 v37, v37, v142
	v_subrev_u32_e32 v142, s11, v37
	v_min_u32_e32 v37, v37, v142
	v_ashrrev_i32_e32 v116, 8, v100
	v_ashrrev_i32_e32 v124, 8, v101
	v_ashrrev_i32_e32 v132, 8, v102
	v_ashrrev_i32_e32 v140, 8, v103
	s_waitcnt lgkmcnt(0)
	v_add_u32_e32 v116, v116, v113
	v_add_u32_e32 v124, v124, v121
	v_add_u32_e32 v132, v132, v129
	v_add_u32_e32 v140, v140, v137
	v_add3_u32 v116, v116, v114, v115
	v_add3_u32 v124, v124, v122, v123
	v_add3_u32 v132, v132, v130, v131
	v_add3_u32 v140, v140, v138, v139
	v_cmp_eq_u32_e32 vcc, s93, v117
	v_add_u32_e32 v1, 0x1e000, v10
	s_and_saveexec_b64 s[24:25], vcc
	global_store_dword v1, v116, s[16:17]
	s_mov_b64 exec, s[24:25]
	v_cmp_eq_u32_e32 vcc, s93, v125
	v_add_u32_e32 v1, 0x1e800, v10
	s_and_saveexec_b64 s[24:25], vcc
	global_store_dword v1, v124, s[16:17]
	s_mov_b64 exec, s[24:25]
	v_cmp_eq_u32_e32 vcc, s93, v133
	v_add_u32_e32 v1, 0x1f000, v10
	s_and_saveexec_b64 s[24:25], vcc
	global_store_dword v1, v132, s[16:17]
	s_mov_b64 exec, s[24:25]
	v_cmp_eq_u32_e32 vcc, s93, v141
	v_add_u32_e32 v1, 0x1f800, v10
	s_and_saveexec_b64 s[24:25], vcc
	global_store_dword v1, v140, s[16:17]
	s_mov_b64 exec, s[24:25]
	v_ashrrev_i32_e32 v113, 8, v116
	v_ashrrev_i32_e32 v121, 8, v124
	v_ashrrev_i32_e32 v129, 8, v132
	v_ashrrev_i32_e32 v137, 8, v140
	v_and_b32_e32 v112, 0xff, v116
	v_and_b32_e32 v120, 0xff, v124
	v_and_b32_e32 v128, 0xff, v132
	v_and_b32_e32 v136, 0xff, v140
	v_lshl_add_u32 v112, v112, 2, s10
	v_lshl_add_u32 v120, v120, 2, s10
	v_lshl_add_u32 v128, v128, 2, s10
	v_lshl_add_u32 v136, v136, 2, s10
	v_add_u32_e32 v114, 0x3c00, v34
	v_add_u32_e32 v122, 0x3d00, v34
	v_add_u32_e32 v130, 0x3e00, v34
	v_add_u32_e32 v138, 0x3f00, v34
	v_mov_b32_e32 v119, -1
	v_mov_b32_e32 v127, -1
	v_mov_b32_e32 v135, -1
	v_mov_b32_e32 v143, -1
	v_cmp_eq_u32_e32 vcc, v113, v2
	v_cmp_eq_u32_e64 s[0:1], v121, v2
	v_cmp_eq_u32_e64 s[6:7], v129, v2
	v_cmp_eq_u32_e64 s[8:9], v137, v2
	v_cndmask_b32_e32 v119, v119, v104, vcc
	v_cndmask_b32_e64 v127, v127, v104, s[0:1]
	v_cndmask_b32_e64 v135, v135, v104, s[6:7]
	v_cndmask_b32_e64 v143, v143, v104, s[8:9]
	v_cmp_eq_u32_e32 vcc, v113, v3
	v_cmp_eq_u32_e64 s[0:1], v121, v3
	v_cmp_eq_u32_e64 s[6:7], v129, v3
	v_cmp_eq_u32_e64 s[8:9], v137, v3
	v_cndmask_b32_e32 v119, v119, v105, vcc
	v_cndmask_b32_e64 v127, v127, v105, s[0:1]
	v_cndmask_b32_e64 v135, v135, v105, s[6:7]
	v_cndmask_b32_e64 v143, v143, v105, s[8:9]
	v_cmp_eq_u32_e32 vcc, v113, v4
	v_cmp_eq_u32_e64 s[0:1], v121, v4
	v_cmp_eq_u32_e64 s[6:7], v129, v4
	v_cmp_eq_u32_e64 s[8:9], v137, v4
	v_cndmask_b32_e32 v119, v119, v106, vcc
	v_cndmask_b32_e64 v127, v127, v106, s[0:1]
	v_cndmask_b32_e64 v135, v135, v106, s[6:7]
	v_cndmask_b32_e64 v143, v143, v106, s[8:9]
	v_cmp_eq_u32_e32 vcc, v113, v5
	v_cmp_eq_u32_e64 s[0:1], v121, v5
	v_cmp_eq_u32_e64 s[6:7], v129, v5
	v_cmp_eq_u32_e64 s[8:9], v137, v5
	v_cndmask_b32_e32 v119, v119, v107, vcc
	v_cndmask_b32_e64 v127, v127, v107, s[0:1]
	v_cndmask_b32_e64 v135, v135, v107, s[6:7]
	v_cndmask_b32_e64 v143, v143, v107, s[8:9]
	v_cmp_gt_i32_e32 vcc, 0, v6
	s_cbranch_vccnz .Lprep_a_m15
	v_cmp_eq_u32_e32 vcc, v113, v6
	v_cmp_eq_u32_e64 s[0:1], v121, v6
	v_cmp_eq_u32_e64 s[6:7], v129, v6
	v_cmp_eq_u32_e64 s[8:9], v137, v6
	v_cndmask_b32_e32 v119, v119, v108, vcc
	v_cndmask_b32_e64 v127, v127, v108, s[0:1]
	v_cndmask_b32_e64 v135, v135, v108, s[6:7]
	v_cndmask_b32_e64 v143, v143, v108, s[8:9]
	v_cmp_eq_u32_e32 vcc, v113, v7
	v_cmp_eq_u32_e64 s[0:1], v121, v7
	v_cmp_eq_u32_e64 s[6:7], v129, v7
	v_cmp_eq_u32_e64 s[8:9], v137, v7
	v_cndmask_b32_e32 v119, v119, v109, vcc
	v_cndmask_b32_e64 v127, v127, v109, s[0:1]
	v_cndmask_b32_e64 v135, v135, v109, s[6:7]
	v_cndmask_b32_e64 v143, v143, v109, s[8:9]
	v_cmp_eq_u32_e32 vcc, v113, v8
	v_cmp_eq_u32_e64 s[0:1], v121, v8
	v_cmp_eq_u32_e64 s[6:7], v129, v8
	v_cmp_eq_u32_e64 s[8:9], v137, v8
	v_cndmask_b32_e32 v119, v119, v110, vcc
	v_cndmask_b32_e64 v127, v127, v110, s[0:1]
	v_cndmask_b32_e64 v135, v135, v110, s[6:7]
	v_cndmask_b32_e64 v143, v143, v110, s[8:9]
	v_cmp_eq_u32_e32 vcc, v113, v9
	v_cmp_eq_u32_e64 s[0:1], v121, v9
	v_cmp_eq_u32_e64 s[6:7], v129, v9
	v_cmp_eq_u32_e64 s[8:9], v137, v9
	v_cndmask_b32_e32 v119, v119, v111, vcc
	v_cndmask_b32_e64 v127, v127, v111, s[0:1]
	v_cndmask_b32_e64 v135, v135, v111, s[6:7]
	v_cndmask_b32_e64 v143, v143, v111, s[8:9]
.Lprep_a_m15:
	v_add_u32_e32 v112, v112, v119
	v_add_u32_e32 v120, v120, v127
	v_add_u32_e32 v128, v128, v135
	v_add_u32_e32 v136, v136, v143
	v_cmp_ne_u32_e32 vcc, -1, v119
	s_and_saveexec_b64 s[24:25], vcc
	ds_write_b32 v112, v114
	s_mov_b64 exec, s[24:25]
	v_cmp_ne_u32_e32 vcc, -1, v127
	s_and_saveexec_b64 s[24:25], vcc
	ds_write_b32 v120, v122
	s_mov_b64 exec, s[24:25]
	v_cmp_ne_u32_e32 vcc, -1, v135
	s_and_saveexec_b64 s[24:25], vcc
	ds_write_b32 v128, v130
	s_mov_b64 exec, s[24:25]
	v_cmp_ne_u32_e32 vcc, -1, v143
	s_and_saveexec_b64 s[24:25], vcc
	ds_write_b32 v136, v138
	s_mov_b64 exec, s[24:25]
	s_mov_b64 s[0:1], 0

.LBB0_1473:
	s_or_b64 exec, exec, s[0:1]
	s_abs_i32 s11, s80
	v_cvt_f32_u32_e32 v1, s11
	v_mov_b32_e32 v11, 0
	s_sub_i32 s0, 0, s11
	s_waitcnt lgkmcnt(0)
	v_rcp_iflag_f32_e32 v2, v1
	s_barrier
	v_lshrrev_b32_e32 v1, 6, v0
	v_mul_f32_e32 v2, 0x4f7ffffe, v2
	v_cvt_u32_f32_e32 v10, v2
	ds_read_b128 v[2:5], v11 offset:37120
	ds_read_b128 v[6:9], v11 offset:37136
	v_lshrrev_b32_e32 v14, 7, v0
	s_movk_i32 s12, 0xfe00
	v_mul_lo_u32 v12, s0, v10
	v_mul_hi_u32 v12, v10, v12
	v_add_u32_e32 v15, v10, v12
	v_lshlrev_b32_e32 v10, 2, v0
	v_lshl_add_u64 v[12:13], s[28:29], 0, v[10:11]
	s_mov_b64 s[0:1], 0x110000
	v_and_b32_e32 v11, 0x180, v0
	v_lshl_add_u64 v[12:13], v[12:13], 0, s[0:1]
	v_add_u32_e32 v11, 0, v11
	s_mov_b64 s[0:1], 0
	s_add_i32 s10, 0, 0x22000
	s_mov_b64 s[6:7], 0x800
	s_movk_i32 s13, 0x7dff
	v_mov_b32_e32 v16, 2
	v_mov_b32_e32 v17, v34
	s_add_u32 s12, s28, 0x110000
	s_addc_u32 s13, s29, 0
	s_add_u32 s16, s28, 0x150000
	s_addc_u32 s17, s29, 0
	v_lshrrev_b32_e32 v36, 7, v0
	v_mov_b32_e32 v104, 0x0
	v_mov_b32_e32 v105, 0x400
	v_mov_b32_e32 v106, 0x800
	v_mov_b32_e32 v107, 0xc00
	v_mov_b32_e32 v108, 0x1000
	v_mov_b32_e32 v109, 0x1400
	v_mov_b32_e32 v110, 0x1800
	v_mov_b32_e32 v111, 0x1c00
	global_load_dword v40, v10, s[12:13]
	v_add_u32_e32 v1, 0x800, v10
	global_load_dword v41, v1, s[12:13]
	v_add_u32_e32 v1, 0x1000, v10
	global_load_dword v42, v1, s[12:13]
	v_add_u32_e32 v1, 0x1800, v10
	global_load_dword v43, v1, s[12:13]
	v_add_u32_e32 v1, 0x2000, v10
	global_load_dword v44, v1, s[12:13]
	v_add_u32_e32 v1, 0x2800, v10
	global_load_dword v45, v1, s[12:13]
	v_add_u32_e32 v1, 0x3000, v10
	global_load_dword v46, v1, s[12:13]
	v_add_u32_e32 v1, 0x3800, v10
	global_load_dword v47, v1, s[12:13]
	v_add_u32_e32 v1, 0x4000, v10
	global_load_dword v48, v1, s[12:13]
	v_add_u32_e32 v1, 0x4800, v10
	global_load_dword v49, v1, s[12:13]
	v_add_u32_e32 v1, 0x5000, v10
	global_load_dword v50, v1, s[12:13]
	v_add_u32_e32 v1, 0x5800, v10
	global_load_dword v51, v1, s[12:13]
	v_add_u32_e32 v1, 0x6000, v10
	global_load_dword v52, v1, s[12:13]
	v_add_u32_e32 v1, 0x6800, v10
	global_load_dword v53, v1, s[12:13]
	v_add_u32_e32 v1, 0x7000, v10
	global_load_dword v54, v1, s[12:13]
	v_add_u32_e32 v1, 0x7800, v10
	global_load_dword v55, v1, s[12:13]
	v_add_u32_e32 v1, 0x8000, v10
	global_load_dword v56, v1, s[12:13]
	v_add_u32_e32 v1, 0x8800, v10
	global_load_dword v57, v1, s[12:13]
	v_add_u32_e32 v1, 0x9000, v10
	global_load_dword v58, v1, s[12:13]
	v_add_u32_e32 v1, 0x9800, v10
	global_load_dword v59, v1, s[12:13]
	v_add_u32_e32 v1, 0xa000, v10
	global_load_dword v60, v1, s[12:13]
	v_add_u32_e32 v1, 0xa800, v10
	global_load_dword v61, v1, s[12:13]
	v_add_u32_e32 v1, 0xb000, v10
	global_load_dword v62, v1, s[12:13]
	v_add_u32_e32 v1, 0xb800, v10
	global_load_dword v63, v1, s[12:13]
	v_add_u32_e32 v1, 0xc000, v10
	global_load_dword v64, v1, s[12:13]
	v_add_u32_e32 v1, 0xc800, v10
	global_load_dword v65, v1, s[12:13]
	v_add_u32_e32 v1, 0xd000, v10
	global_load_dword v66, v1, s[12:13]
	v_add_u32_e32 v1, 0xd800, v10
	global_load_dword v67, v1, s[12:13]
	v_add_u32_e32 v1, 0xe000, v10
	global_load_dword v68, v1, s[12:13]
	v_add_u32_e32 v1, 0xe800, v10
	global_load_dword v69, v1, s[12:13]
	v_add_u32_e32 v1, 0xf000, v10
	global_load_dword v70, v1, s[12:13]
	v_add_u32_e32 v1, 0xf800, v10
	global_load_dword v71, v1, s[12:13]
	v_add_u32_e32 v1, 0x10000, v10
	global_load_dword v72, v1, s[12:13]
	v_add_u32_e32 v1, 0x10800, v10
	global_load_dword v73, v1, s[12:13]
	v_add_u32_e32 v1, 0x11000, v10
	global_load_dword v74, v1, s[12:13]
	v_add_u32_e32 v1, 0x11800, v10
	global_load_dword v75, v1, s[12:13]
	v_add_u32_e32 v1, 0x12000, v10
	global_load_dword v76, v1, s[12:13]
	v_add_u32_e32 v1, 0x12800, v10
	global_load_dword v77, v1, s[12:13]
	v_add_u32_e32 v1, 0x13000, v10
	global_load_dword v78, v1, s[12:13]
	v_add_u32_e32 v1, 0x13800, v10
	global_load_dword v79, v1, s[12:13]
	v_add_u32_e32 v1, 0x14000, v10
	global_load_dword v80, v1, s[12:13]
	v_add_u32_e32 v1, 0x14800, v10
	global_load_dword v81, v1, s[12:13]
	v_add_u32_e32 v1, 0x15000, v10
	global_load_dword v82, v1, s[12:13]
	v_add_u32_e32 v1, 0x15800, v10
	global_load_dword v83, v1, s[12:13]
	v_add_u32_e32 v1, 0x16000, v10
	global_load_dword v84, v1, s[12:13]
	v_add_u32_e32 v1, 0x16800, v10
	global_load_dword v85, v1, s[12:13]
	v_add_u32_e32 v1, 0x17000, v10
	global_load_dword v86, v1, s[12:13]
	v_add_u32_e32 v1, 0x17800, v10
	global_load_dword v87, v1, s[12:13]
	s_waitcnt vmcnt(32)
	v_add_u32_e32 v1, 0x18000, v10
	global_load_dword v88, v1, s[12:13]
	v_add_u32_e32 v1, 0x18800, v10
	global_load_dword v89, v1, s[12:13]
	v_add_u32_e32 v1, 0x19000, v10
	global_load_dword v90, v1, s[12:13]
	v_add_u32_e32 v1, 0x19800, v10
	global_load_dword v91, v1, s[12:13]
	v_add_u32_e32 v1, 0x1a000, v10
	global_load_dword v92, v1, s[12:13]
	v_add_u32_e32 v1, 0x1a800, v10
	global_load_dword v93, v1, s[12:13]
	v_add_u32_e32 v1, 0x1b000, v10
	global_load_dword v94, v1, s[12:13]
	v_add_u32_e32 v1, 0x1b800, v10
	global_load_dword v95, v1, s[12:13]
	v_add_u32_e32 v1, 0x1c000, v10
	global_load_dword v96, v1, s[12:13]
	v_add_u32_e32 v1, 0x1c800, v10
	global_load_dword v97, v1, s[12:13]
	v_add_u32_e32 v1, 0x1d000, v10
	global_load_dword v98, v1, s[12:13]
	v_add_u32_e32 v1, 0x1d800, v10
	global_load_dword v99, v1, s[12:13]
	v_add_u32_e32 v1, 0x1e000, v10
	global_load_dword v100, v1, s[12:13]
	v_add_u32_e32 v1, 0x1e800, v10
	global_load_dword v101, v1, s[12:13]
	v_add_u32_e32 v1, 0x1f000, v10
	global_load_dword v102, v1, s[12:13]
	v_add_u32_e32 v1, 0x1f800, v10
	global_load_dword v103, v1, s[12:13]
	s_waitcnt lgkmcnt(0)
	v_mul_hi_u32 v37, v36, v15
	v_mul_lo_u32 v37, v37, s11
	v_sub_u32_e32 v37, v36, v37
	v_subrev_u32_e32 v1, s11, v37
	v_min_u32_e32 v37, v37, v1
	v_subrev_u32_e32 v1, s11, v37
	v_min_u32_e32 v37, v37, v1
	s_waitcnt vmcnt(0)
	v_and_b32_e32 v112, 0xff, v40
	v_and_b32_e32 v120, 0xff, v41
	v_and_b32_e32 v128, 0xff, v42
	v_and_b32_e32 v136, 0xff, v43
	v_lshlrev_b32_e32 v112, 2, v112
	v_lshlrev_b32_e32 v120, 2, v120
	v_lshlrev_b32_e32 v128, 2, v128
	v_lshlrev_b32_e32 v136, 2, v136
	v_add_u32_e32 v118, v112, v11
	v_add_u32_e32 v126, v120, v11
	v_add_u32_e32 v134, v128, v11
	v_add_u32_e32 v142, v136, v11
	ds_read_b32 v113, v112 offset:36864
	ds_read_b32 v114, v112 offset:34816
	ds_read_b32 v115, v118
	ds_read_b32 v121, v120 offset:36864
	ds_read_b32 v122, v120 offset:34816
	ds_read_b32 v123, v126 offset:512
	ds_read_b32 v129, v128 offset:36864
	ds_read_b32 v130, v128 offset:34816
	ds_read_b32 v131, v134 offset:1024
	ds_read_b32 v137, v136 offset:36864
	ds_read_b32 v138, v136 offset:34816
	ds_read_b32 v139, v142 offset:1536
	v_mov_b32_e32 v117, v37
	v_add_u32_e32 v37, 4, v37
	v_subrev_u32_e32 v118, s11, v37
	v_min_u32_e32 v37, v37, v118
	v_subrev_u32_e32 v118, s11, v37
	v_min_u32_e32 v37, v37, v118
	v_mov_b32_e32 v125, v37
	v_add_u32_e32 v37, 4, v37
	v_subrev_u32_e32 v126, s11, v37
	v_min_u32_e32 v37, v37, v126
	v_subrev_u32_e32 v126, s11, v37
	v_min_u32_e32 v37, v37, v126
	v_mov_b32_e32 v133, v37
	v_add_u32_e32 v37, 4, v37
	v_subrev_u32_e32 v134, s11, v37
	v_min_u32_e32 v37, v37, v134
	v_subrev_u32_e32 v134, s11, v37
	v_min_u32_e32 v37, v37, v134
	v_mov_b32_e32 v141, v37
	v_add_u32_e32 v37, 4, v37
	v_subrev_u32_e32 v142, s11, v37
	v_min_u32_e32 v37, v37, v142
	v_subrev_u32_e32 v142, s11, v37
	v_min_u32_e32 v37, v37, v142
	v_ashrrev_i32_e32 v116, 8, v40
	v_ashrrev_i32_e32 v124, 8, v41
	v_ashrrev_i32_e32 v132, 8, v42
	v_ashrrev_i32_e32 v140, 8, v43
	s_waitcnt lgkmcnt(0)
	v_add_u32_e32 v116, v116, v113
	v_add_u32_e32 v124, v124, v121
	v_add_u32_e32 v132, v132, v129
	v_add_u32_e32 v140, v140, v137
	v_add3_u32 v116, v116, v114, v115
	v_add3_u32 v124, v124, v122, v123
	v_add3_u32 v132, v132, v130, v131
	v_add3_u32 v140, v140, v138, v139
	v_cmp_eq_u32_e32 vcc, s93, v117
	v_mov_b32_e32 v1, v10
	s_and_saveexec_b64 s[24:25], vcc
	global_store_dword v1, v116, s[16:17]
	s_mov_b64 exec, s[24:25]
	v_cmp_eq_u32_e32 vcc, s93, v125
	v_add_u32_e32 v1, 0x800, v10
	s_and_saveexec_b64 s[24:25], vcc
	global_store_dword v1, v124, s[16:17]
	s_mov_b64 exec, s[24:25]
	v_cmp_eq_u32_e32 vcc, s93, v133
	v_add_u32_e32 v1, 0x1000, v10
	s_and_saveexec_b64 s[24:25], vcc
	global_store_dword v1, v132, s[16:17]
	s_mov_b64 exec, s[24:25]
	v_cmp_eq_u32_e32 vcc, s93, v141
	v_add_u32_e32 v1, 0x1800, v10
	s_and_saveexec_b64 s[24:25], vcc
	global_store_dword v1, v140, s[16:17]
	s_mov_b64 exec, s[24:25]
	v_ashrrev_i32_e32 v113, 8, v116
	v_ashrrev_i32_e32 v121, 8, v124
	v_ashrrev_i32_e32 v129, 8, v132
	v_ashrrev_i32_e32 v137, 8, v140
	v_and_b32_e32 v112, 0xff, v116
	v_and_b32_e32 v120, 0xff, v124
	v_and_b32_e32 v128, 0xff, v132
	v_and_b32_e32 v136, 0xff, v140
	v_lshl_add_u32 v112, v112, 2, s10
	v_lshl_add_u32 v120, v120, 2, s10
	v_lshl_add_u32 v128, v128, 2, s10
	v_lshl_add_u32 v136, v136, 2, s10
	v_mov_b32_e32 v114, v34
	v_add_u32_e32 v122, 0x100, v34
	v_add_u32_e32 v130, 0x200, v34
	v_add_u32_e32 v138, 0x300, v34
	v_mov_b32_e32 v119, -1
	v_mov_b32_e32 v127, -1
	v_mov_b32_e32 v135, -1
	v_mov_b32_e32 v143, -1
	v_cmp_eq_u32_e32 vcc, v113, v2
	v_cmp_eq_u32_e64 s[0:1], v121, v2
	v_cmp_eq_u32_e64 s[6:7], v129, v2
	v_cmp_eq_u32_e64 s[8:9], v137, v2
	v_cndmask_b32_e32 v119, v119, v104, vcc
	v_cndmask_b32_e64 v127, v127, v104, s[0:1]
	v_cndmask_b32_e64 v135, v135, v104, s[6:7]
	v_cndmask_b32_e64 v143, v143, v104, s[8:9]
	v_cmp_eq_u32_e32 vcc, v113, v3
	v_cmp_eq_u32_e64 s[0:1], v121, v3
	v_cmp_eq_u32_e64 s[6:7], v129, v3
	v_cmp_eq_u32_e64 s[8:9], v137, v3
	v_cndmask_b32_e32 v119, v119, v105, vcc
	v_cndmask_b32_e64 v127, v127, v105, s[0:1]
	v_cndmask_b32_e64 v135, v135, v105, s[6:7]
	v_cndmask_b32_e64 v143, v143, v105, s[8:9]
	v_cmp_eq_u32_e32 vcc, v113, v4
	v_cmp_eq_u32_e64 s[0:1], v121, v4
	v_cmp_eq_u32_e64 s[6:7], v129, v4
	v_cmp_eq_u32_e64 s[8:9], v137, v4
	v_cndmask_b32_e32 v119, v119, v106, vcc
	v_cndmask_b32_e64 v127, v127, v106, s[0:1]
	v_cndmask_b32_e64 v135, v135, v106, s[6:7]
	v_cndmask_b32_e64 v143, v143, v106, s[8:9]
	v_cmp_eq_u32_e32 vcc, v113, v5
	v_cmp_eq_u32_e64 s[0:1], v121, v5
	v_cmp_eq_u32_e64 s[6:7], v129, v5
	v_cmp_eq_u32_e64 s[8:9], v137, v5
	v_cndmask_b32_e32 v119, v119, v107, vcc
	v_cndmask_b32_e64 v127, v127, v107, s[0:1]
	v_cndmask_b32_e64 v135, v135, v107, s[6:7]
	v_cndmask_b32_e64 v143, v143, v107, s[8:9]
	v_cmp_gt_i32_e32 vcc, 0, v6
	s_cbranch_vccnz .Lprep_b_m0
	v_cmp_eq_u32_e32 vcc, v113, v6
	v_cmp_eq_u32_e64 s[0:1], v121, v6
	v_cmp_eq_u32_e64 s[6:7], v129, v6
	v_cmp_eq_u32_e64 s[8:9], v137, v6
	v_cndmask_b32_e32 v119, v119, v108, vcc
	v_cndmask_b32_e64 v127, v127, v108, s[0:1]
	v_cndmask_b32_e64 v135, v135, v108, s[6:7]
	v_cndmask_b32_e64 v143, v143, v108, s[8:9]
	v_cmp_eq_u32_e32 vcc, v113, v7
	v_cmp_eq_u32_e64 s[0:1], v121, v7
	v_cmp_eq_u32_e64 s[6:7], v129, v7
	v_cmp_eq_u32_e64 s[8:9], v137, v7
	v_cndmask_b32_e32 v119, v119, v109, vcc
	v_cndmask_b32_e64 v127, v127, v109, s[0:1]
	v_cndmask_b32_e64 v135, v135, v109, s[6:7]
	v_cndmask_b32_e64 v143, v143, v109, s[8:9]
	v_cmp_eq_u32_e32 vcc, v113, v8
	v_cmp_eq_u32_e64 s[0:1], v121, v8
	v_cmp_eq_u32_e64 s[6:7], v129, v8
	v_cmp_eq_u32_e64 s[8:9], v137, v8
	v_cndmask_b32_e32 v119, v119, v110, vcc
	v_cndmask_b32_e64 v127, v127, v110, s[0:1]
	v_cndmask_b32_e64 v135, v135, v110, s[6:7]
	v_cndmask_b32_e64 v143, v143, v110, s[8:9]
	v_cmp_eq_u32_e32 vcc, v113, v9
	v_cmp_eq_u32_e64 s[0:1], v121, v9
	v_cmp_eq_u32_e64 s[6:7], v129, v9
	v_cmp_eq_u32_e64 s[8:9], v137, v9
	v_cndmask_b32_e32 v119, v119, v111, vcc
	v_cndmask_b32_e64 v127, v127, v111, s[0:1]
	v_cndmask_b32_e64 v135, v135, v111, s[6:7]
	v_cndmask_b32_e64 v143, v143, v111, s[8:9]
